# recurrence pass B: bf16-packed MFMA accumulators feed the next step's B operand directly (P stored column-permuted by pass A), no LDS round trip in the serial chain
# baseline (speedup 1.0000x reference)
; DI void phase_chunkA(const Args& a, LAS unsigned char* lds, int wave, int lane, int tid, int bid, int G) {
;     ...
;           for (int e = 0; e < 8; ++e) gp[e] = gv[e] / wv[e];
;           if (t == CK - 1) {
; #pragma unroll
;               for (int e = 0; e < 8; ++e) gC[c8 + e] = gv[e]; } }
;         {
;           float rt[8], at[8], kt[8], bt[8], vv[8];
; #pragma unroll
;           for (int e = 0; e < 8; ++e) { const unsigned rw = (e < 2) ? r8.x : (e < 4) ? r8.y : (e < 6) ? r8.z : r8.w, kw = (e < 2) ? k8.x : (e < 4) ? k8.y : (e < 6) ? k8.z : k8.w, vw = (e < 2) ? v8.x : (e < 4) ? v8.y : (e < 6) ? v8.z : v8.w,
;                   qw = (e < 2) ? kk8.x : (e < 4) ? kk8.y : (e < 6) ? kk8.z : kk8.w, bw = (e < 2) ? b8.x : (e < 4) ? b8.y : (e < 6) ? b8.z : b8.w;
;               const float rv = (e & 1) ? bfhi(rw) : bflo(rw), kv = (e & 1) ? bfhi(kw) : bflo(kw), vx = (e & 1) ? bfhi(vw) : bflo(vw), qv = (e & 1) ? bfhi(qw) : bflo(qw), bv = (e & 1) ? bfhi(bw) : bflo(bw);
;               const float ig = 1.f / gv[e];
;               rt[e] = rv * gv[e]; at[e] = -qv * gp[e]; kt[e] = kv * ig; bt[e] = bv * ig; vv[e] = vx; }
;           *(LAS u32x4*)(SL(6) + t * CP + c8) = (u32x4){pk2(rt[0], rt[1]), pk2(rt[2], rt[3]), pk2(rt[4], rt[5]), pk2(rt[6], rt[7])};
;           *(LAS u32x4*)(SL(0) + t * CP + c8) = (u32x4){pk2(at[0], at[1]), pk2(at[2], at[3]), pk2(at[4], at[5]), pk2(at[6], at[7])};
;           *(LAS u32x4*)(SL(4) + t * CP + c8) = (u32x4){pk2(kt[0], kt[1]), pk2(kt[2], kt[3]), pk2(kt[4], kt[5]), pk2(kt[6], kt[7])};
;           *(LAS u32x4*)(SL(2) + t * CP + c8) = (u32x4){pk2(bt[0], bt[1]), pk2(bt[2], bt[3]), pk2(bt[4], bt[5]), pk2(bt[6], bt[7])};
;           *(LAS u32x4*)(SL(10) + t * CP + c8) = (u32x4){pk2(vv[0], vv[1]), pk2(vv[2], vv[3]), pk2(vv[4], vv[5]), pk2(vv[6], vv[7])};
;           { unsigned iw[4];
; #pragma unroll
;             for (int e = 0; e < 4; ++e) iw[e] = ((c8 + 2 * e == t) ? 0x3f80u : 0u) | ((c8 + 2 * e + 1 == t) ? 0x3f800000u : 0u);
;             *(LAS u32x4*)(SL(11) + t * CP + c8) = (u32x4){iw[0], iw[1], iw[2], iw[3]}; } }
;         CK_BAR();
;     ...
;         { auto t1 = [&](int m, int n, f32x4 v) { ck_wr_tr(SL(1), m, n, v); }; auto t3 = [&](int m, int n, f32x4 v) { ck_wr_tr(SL(3), m, n, v); };
;           auto t5 = [&](int m, int n, f32x4 v) { ck_wr_tr(SL(5), m, n, v); }; auto t7 = [&](int m, int n, f32x4 v) { ck_wr_tr(SL(7), m, n, v); };
.LBB0_1017:
	s_or_b64 exec, exec, s[2:3]
	v_lshlrev_b32_e32 v84, 16, v42
	v_and_b32_e32 v85, 0xffff0000, v42
	v_lshlrev_b32_e32 v90, 16, v43
	v_rcp_f32_e32 v78, v59
	s_nop 0
	v_mul_f32_e32 v79, v67, v78
	v_and_b32_e32 v92, 0xffff0000, v43
	v_lshlrev_b32_e32 v93, 16, v45
	v_and_b32_e32 v144, 0xffff0000, v45
	v_rcp_f32_e32 v59, v58
	s_nop 0
	v_mul_f32_e32 v78, v66, v59
	v_rcp_f32_e32 v58, v61
	s_nop 0
	v_mul_f32_e32 v61, v69, v58
	v_rcp_f32_e32 v58, v60
	s_nop 0
	v_mul_f32_e32 v60, v68, v58
	v_rcp_f32_e32 v58, v55
	s_nop 0
	v_mul_f32_e32 v59, v63, v58
	v_rcp_f32_e32 v55, v54
	s_nop 0
	v_mul_f32_e32 v58, v62, v55
	v_rcp_f32_e32 v54, v57
	s_nop 0
	v_mul_f32_e32 v55, v65, v54
	v_rcp_f32_e32 v54, v56
	s_nop 0
	v_mul_f32_e32 v54, v64, v54
	v_rcp_f32_e32 v57, v67
	v_lshlrev_b32_e32 v80, 16, v34
	v_and_b32_e32 v81, 0xffff0000, v34
	v_rcp_f32_e32 v56, v66
	v_pk_mul_f32 v[80:81], v[66:67], v[80:81]
	v_lshlrev_b32_e32 v66, 16, v46
	v_and_b32_e32 v67, 0xffff0000, v46
	v_pk_mul_f32 v[78:79], v[78:79], v[66:67] neg_lo:[0,1] neg_hi:[0,1]
	v_lshlrev_b32_e32 v66, 16, v38
	v_and_b32_e32 v67, 0xffff0000, v38
	v_lshlrev_b32_e32 v82, 16, v50
	v_and_b32_e32 v83, 0xffff0000, v50
	v_pk_mul_f32 v[66:67], v[56:57], v[66:67]
	v_pk_mul_f32 v[56:57], v[56:57], v[82:83]
	v_rcp_f32_e32 v83, v69
	v_rcp_f32_e32 v82, v68
	v_lshlrev_b32_e32 v34, 16, v35
	v_and_b32_e32 v35, 0xffff0000, v35
	v_pk_mul_f32 v[42:43], v[68:69], v[34:35]
	v_lshlrev_b32_e32 v34, 16, v47
	v_and_b32_e32 v35, 0xffff0000, v47
	v_pk_mul_f32 v[46:47], v[60:61], v[34:35] neg_lo:[0,1] neg_hi:[0,1]
	v_lshlrev_b32_e32 v34, 16, v39
	v_and_b32_e32 v35, 0xffff0000, v39
	v_pk_mul_f32 v[38:39], v[82:83], v[34:35]
	v_lshlrev_b32_e32 v34, 16, v51
	v_and_b32_e32 v35, 0xffff0000, v51
	v_pk_mul_f32 v[50:51], v[82:83], v[34:35]
	v_lshlrev_b32_e32 v82, 16, v44
	v_and_b32_e32 v83, 0xffff0000, v44
	v_rcp_f32_e32 v35, v63
	v_lshlrev_b32_e32 v60, 16, v36
	v_and_b32_e32 v61, 0xffff0000, v36
	v_rcp_f32_e32 v34, v62
	v_pk_mul_f32 v[60:61], v[62:63], v[60:61]
	v_lshlrev_b32_e32 v62, 16, v48
	v_and_b32_e32 v63, 0xffff0000, v48
	v_pk_mul_f32 v[58:59], v[58:59], v[62:63] neg_lo:[0,1] neg_hi:[0,1]
	v_lshlrev_b32_e32 v62, 16, v40
	v_and_b32_e32 v63, 0xffff0000, v40
	v_lshlrev_b32_e32 v68, 16, v52
	v_and_b32_e32 v69, 0xffff0000, v52
	v_pk_mul_f32 v[62:63], v[34:35], v[62:63]
	v_pk_mul_f32 v[68:69], v[34:35], v[68:69]
	v_rcp_f32_e32 v35, v65
	v_lshlrev_b32_e32 v36, 16, v37
	v_and_b32_e32 v37, 0xffff0000, v37
	v_pk_mul_f32 v[44:45], v[64:65], v[36:37]
	v_lshlrev_b32_e32 v36, 16, v49
	v_and_b32_e32 v37, 0xffff0000, v49
	v_rcp_f32_e32 v34, v64
	v_pk_mul_f32 v[48:49], v[54:55], v[36:37] neg_lo:[0,1] neg_hi:[0,1]
	v_lshlrev_b32_e32 v36, 16, v41
	v_and_b32_e32 v37, 0xffff0000, v41
	v_pk_mul_f32 v[40:41], v[34:35], v[36:37]
	v_lshlrev_b32_e32 v36, 16, v53
	v_and_b32_e32 v37, 0xffff0000, v53
	v_pk_mul_f32 v[52:53], v[34:35], v[36:37]
	v_cvt_pk_bf16_f32 v34, v80, v81
	v_cvt_pk_bf16_f32 v35, v42, v43
	v_cvt_pk_bf16_f32 v36, v60, v61
	v_cvt_pk_bf16_f32 v37, v44, v45
	ds_write_b128 v89, v[34:37] offset:55296
	v_cvt_pk_bf16_f32 v34, v78, v79
	v_cvt_pk_bf16_f32 v35, v46, v47
	v_cvt_pk_bf16_f32 v36, v58, v59
	v_cvt_pk_bf16_f32 v37, v48, v49
	ds_write_b128 v89, v[34:37]
	v_cvt_pk_bf16_f32 v34, v66, v67
	v_cvt_pk_bf16_f32 v35, v38, v39
	v_cvt_pk_bf16_f32 v36, v62, v63
	v_cvt_pk_bf16_f32 v37, v40, v41
	ds_write_b128 v89, v[34:37] offset:36864
	v_cvt_pk_bf16_f32 v34, v56, v57
	v_cvt_pk_bf16_f32 v35, v50, v51
	v_cvt_pk_bf16_f32 v36, v68, v69
	v_cvt_pk_bf16_f32 v37, v52, v53
	ds_write_b128 v89, v[34:37] offset:18432
	v_cvt_pk_bf16_f32 v34, v84, v85
	v_cvt_pk_bf16_f32 v35, v90, v92
	v_cvt_pk_bf16_f32 v36, v82, v83
	v_cvt_pk_bf16_f32 v37, v93, v144
	ds_write_b128 v94, v[34:37]
	ds_write_b128 v95, v[2:5]
	s_waitcnt lgkmcnt(0)
	s_barrier
	ds_read_b128 v[34:37], v97
	ds_read_b128 v[38:41], v142
	ds_read_b128 v[42:45], v142 offset:2304
	ds_read_b128 v[46:49], v97 offset:64
	ds_read_b128 v[50:53], v142 offset:64
	ds_read_b128 v[54:57], v142 offset:2368
	ds_read_b128 v[58:61], v97 offset:18432
	ds_read_b128 v[62:65], v97 offset:18496
	s_waitcnt lgkmcnt(6)
	v_mfma_f32_16x16x32_bf16 v[66:69], v[34:37], v[38:41], 0
	s_waitcnt lgkmcnt(5)
	v_mfma_f32_16x16x32_bf16 v[34:37], v[34:37], v[42:45], 0
	s_waitcnt lgkmcnt(2)
	v_mfma_f32_16x16x32_bf16 v[34:37], v[46:49], v[54:57], v[34:37]
	s_waitcnt lgkmcnt(1)
	v_mfma_f32_16x16x32_bf16 v[38:41], v[58:61], v[38:41], 0
	v_mfma_f32_16x16x32_bf16 v[42:45], v[58:61], v[42:45], 0
	s_nop 4
	v_cvt_pk_bf16_f32 v34, v34, v35
	v_cvt_pk_bf16_f32 v35, v36, v37
	ds_write_b64 v99, v[34:35] offset:11520
	s_waitcnt lgkmcnt(1)
	v_mfma_f32_16x16x32_bf16 v[34:37], v[62:65], v[50:53], v[38:41]
	v_mfma_f32_16x16x32_bf16 v[66:69], v[46:49], v[50:53], v[66:69]
	s_nop 6
	v_cvt_pk_bf16_f32 v34, v34, v35
	v_cvt_pk_bf16_f32 v35, v36, v37
	ds_write_b64 v99, v[34:35] offset:27648
	v_mfma_f32_16x16x32_bf16 v[34:37], v[62:65], v[54:57], v[42:45]
	v_cvt_pk_bf16_f32 v46, v66, v67
	v_cvt_pk_bf16_f32 v47, v68, v69
	ds_write_b64 v99, v[46:47] offset:9216
	s_nop 4
	v_cvt_pk_bf16_f32 v34, v34, v35
	v_cvt_pk_bf16_f32 v35, v36, v37
	ds_write_b64 v99, v[34:35] offset:29952
	ds_read_b128 v[34:37], v97 offset:36864
	ds_read_b128 v[38:41], v97 offset:36928
	ds_read_b128 v[42:45], v142
	ds_read_b128 v[46:49], v142 offset:64
	ds_read_b128 v[50:53], v142 offset:2304
	ds_read_b128 v[54:57], v142 offset:2368
	ds_read_b128 v[58:61], v101
	ds_read_b128 v[62:65], v101 offset:64
	s_waitcnt lgkmcnt(5)
	v_mfma_f32_16x16x32_bf16 v[66:69], v[34:37], v[42:45], 0
	s_waitcnt lgkmcnt(3)
	v_mfma_f32_16x16x32_bf16 v[34:37], v[34:37], v[50:53], 0
	s_waitcnt lgkmcnt(2)
	v_mfma_f32_16x16x32_bf16 v[34:37], v[38:41], v[54:57], v[34:37]
	v_mfma_f32_16x16x32_bf16 v[66:69], v[38:41], v[46:49], v[66:69]
	s_waitcnt lgkmcnt(1)
	v_mfma_f32_16x16x32_bf16 v[38:41], v[58:61], v[42:45], 0
	s_nop 4
	v_cvt_pk_bf16_f32 v34, v34, v35
	v_cvt_pk_bf16_f32 v35, v36, v37
	v_cvt_pk_bf16_f32 v42, v66, v67
	v_cvt_pk_bf16_f32 v43, v68, v69
	ds_write_b64 v99, v[34:35] offset:48384
	s_waitcnt lgkmcnt(1)
	v_mfma_f32_16x16x32_bf16 v[34:37], v[62:65], v[46:49], v[38:41]
	ds_write_b64 v99, v[42:43] offset:46080
	v_mfma_f32_16x16x32_bf16 v[42:45], v[58:61], v[50:53], 0
	s_nop 5
	v_cvt_pk_bf16_f32 v34, v34, v35
	v_cvt_pk_bf16_f32 v35, v36, v37
	ds_write_b64 v99, v[34:35] offset:64512
	v_mfma_f32_16x16x32_bf16 v[34:37], v[62:65], v[54:57], v[42:45]
	s_nop 7
	v_cvt_pk_bf16_f32 v34, v34, v35
	v_cvt_pk_bf16_f32 v35, v36, v37
	ds_write_b64 v102, v[34:35]
	s_waitcnt lgkmcnt(0)
	s_barrier
; DI void ck_wr_tr(LAS bf16* XT, int m, int n, f32x4 v) { *(LAS u32x2*)(XT + n * CP + m) = (u32x2){pk2(v[0], v[1]), pk2(v[2], v[3])}; }
; #define CK_RUN2(A1, B1, E1, A2, B2, E2) do { CkF f1_, f2_; ck_ld(f1_, A1, B1, wave, lane); ck_ld(f2_, A2, B2, wave, lane); __builtin_amdgcn_sched_barrier(0); \
;             f32x4 c1_[2] = CK_Z2, c2_[2] = CK_Z2; ck_mma(c1_, f1_); ck_mma(c2_, f2_); ck_epi(c1_, wave, lane, E1); ck_epi(c2_, wave, lane, E2); } while (0)
; DI void phase_chunkA(const Args& a, LAS unsigned char* lds, int wave, int lane, int tid, int bid, int G) {
;     ...
;         { auto ePT = [&](int m, int n, f32x4 v) {
; #pragma unroll
;               for (int g = 0; g < 4; ++g) v[g] = (n < m + g) ? v[g] : 0.f;
;               ck_wr_tr(SL(13), m, n, v); };
;           auto ePA = [&](int m, int n, f32x4 v) { f32x4 tt;
; #pragma unroll
;               for (int g = 0; g < 4; ++g) { v[g] = (m + g < n) ? v[g] : 0.f; tt[g] = (m + g == n) ? 1.f : v[g]; }
;               ck_wr_tr(SL(12), m, n, v); ck_wr_tr(SL(8), m, n, tt); };
;           auto eMak = [&](int m, int n, f32x4 v) {
; #pragma unroll
;               for (int g = 0; g < 4; ++g) v[g] = (m + g < n) ? v[g] : 0.f;
;               ck_wr_tr(SL(9), m, n, v); };
;           CK_RUN3(SL(0), SL(2), ePT, SL(2), SL(0), ePA, SL(4), SL(0), eMak); }
;         { auto eNrb = [&](int m, int n, f32x4 v) {
; #pragma unroll
;               for (int g = 0; g < 4; ++g) v[g] = (m + g <= n) ? v[g] : 0.f;
;               ck_wr_tr(SL(10), m, n, v); };
;           auto eNrk = [&](int m, int n, f32x4 v) {
; #pragma unroll
;               for (int g = 0; g < 4; ++g) v[g] = (m + g <= n) ? v[g] : 0.f;
;               ck_wr_tr(SL(11), m, n, v); };
;           CK_RUN2(SL(2), SL(6), eNrb, SL(4), SL(6), eNrk); }
	v_add_u32_e32 v34, v96, v98
	ds_read_b128 v[36:39], v97
	ds_read_b128 v[40:43], v97 offset:64
	ds_read_b128 v[44:47], v34 offset:18432
	ds_read_b128 v[48:51], v34 offset:18496
	ds_read_b128 v[52:55], v34 offset:20736
	ds_read_b128 v[56:59], v34 offset:20800
	ds_read_b128 v[60:63], v97 offset:18432
	ds_read_b128 v[64:67], v97 offset:18496
	ds_read_b128 v[78:81], v34
	ds_read_b128 v[82:85], v34 offset:64
	ds_read_b128 v[144:147], v34 offset:2304
	ds_read_b128 v[148:151], v34 offset:2368
	ds_read_b128 v[152:155], v97 offset:36864
	ds_read_b128 v[156:159], v97 offset:36928
	s_waitcnt lgkmcnt(11)
	v_mfma_f32_16x16x32_bf16 v[44:47], v[36:39], v[44:47], 0
	s_waitcnt lgkmcnt(9)
	v_mfma_f32_16x16x32_bf16 v[36:39], v[36:39], v[52:55], 0
	v_mfma_f32_16x16x32_bf16 v[44:47], v[40:43], v[48:51], v[44:47]
	s_waitcnt lgkmcnt(8)
	v_mfma_f32_16x16x32_bf16 v[36:39], v[40:43], v[56:59], v[36:39]
	s_nop 5
	v_cndmask_b32_e64 v35, 0, v44, s[48:49]
	v_cndmask_b32_e64 v44, v45, 0, s[50:51]
	v_cvt_pk_bf16_f32 v44, v35, v44
	v_cndmask_b32_e64 v35, 0, v36, s[56:57]
	v_cndmask_b32_e64 v40, v37, 0, s[58:59]
	v_cndmask_b32_e64 v41, 0, v38, s[60:61]
	v_cndmask_b32_e64 v42, 0, v39, s[62:63]
	s_waitcnt lgkmcnt(5)
	v_mfma_f32_16x16x32_bf16 v[36:39], v[60:63], v[78:81], 0
	v_cndmask_b32_e64 v45, 0, v46, s[52:53]
	v_cndmask_b32_e64 v46, 0, v47, s[54:55]
	v_cvt_pk_bf16_f32 v45, v45, v46
	s_waitcnt lgkmcnt(4)
	v_mfma_f32_16x16x32_bf16 v[36:39], v[64:67], v[82:85], v[36:39]
	v_cvt_pk_bf16_f32 v40, v35, v40
	v_cvt_pk_bf16_f32 v41, v41, v42
	ds_write_b64 v103, v[44:45]
	ds_write_b64 v104, v[40:41]
	s_waitcnt lgkmcnt(5)
	v_mfma_f32_16x16x32_bf16 v[40:43], v[60:63], v[144:147], 0
	s_nop 1
	v_cndmask_b32_e64 v35, 0, v36, s[50:51]
	v_cndmask_b32_e64 v36, 0, v37, s[64:65]
	v_cndmask_b32_e64 v45, 0, v38, s[66:67]
	v_cndmask_b32_e64 v49, 0, v39, s[68:69]
	v_cndmask_b32_e64 v46, v35, 1.0, s[76:77]
	v_cndmask_b32_e64 v47, v36, 1.0, s[78:79]
	v_cndmask_b32_e64 v48, v45, 1.0, s[80:81]
	v_cndmask_b32_e64 v50, v49, 1.0, s[82:83]
	v_cvt_pk_bf16_f32 v44, v35, v36
	v_cvt_pk_bf16_f32 v45, v45, v49
	s_waitcnt lgkmcnt(4)
	v_mfma_f32_16x16x32_bf16 v[36:39], v[64:67], v[148:151], v[40:43]
	ds_write_b64 v105, v[44:45]
	v_cvt_pk_bf16_f32 v44, v46, v47
	v_cvt_pk_bf16_f32 v45, v48, v50
	s_waitcnt lgkmcnt(4)
	v_mfma_f32_16x16x32_bf16 v[40:43], v[152:155], v[78:81], 0
	ds_write_b64 v107, v[44:45]
	s_nop 1
	v_cndmask_b32_e64 v35, 0, v36, s[58:59]
	v_cndmask_b32_e64 v49, 0, v37, s[70:71]
	v_mfma_f32_16x16x32_bf16 v[44:47], v[152:155], v[144:147], 0
	v_cndmask_b32_e64 v51, 0, v38, s[72:73]
	v_cndmask_b32_e64 v53, 0, v39, s[74:75]
	v_cndmask_b32_e64 v48, v35, 1.0, s[84:85]
	s_waitcnt lgkmcnt(4)
	v_mfma_f32_16x16x32_bf16 v[40:43], v[156:159], v[82:85], v[40:43]
	v_cndmask_b32_e64 v50, v49, 1.0, s[86:87]
	v_cndmask_b32_e64 v52, v51, 1.0, s[88:89]
	v_mfma_f32_16x16x32_bf16 v[36:39], v[156:159], v[148:151], v[44:47]
	s_nop 2
	v_cvt_pk_bf16_f32 v44, v35, v49
	s_nop 0
	v_cndmask_b32_e64 v35, 0, v40, s[50:51]
	v_cndmask_b32_e64 v40, 0, v41, s[64:65]
	v_cndmask_b32_e64 v46, v53, 1.0, s[90:91]
	v_cvt_pk_bf16_f32 v45, v51, v53
	v_cndmask_b32_e64 v41, 0, v42, s[66:67]
	v_cndmask_b32_e64 v42, 0, v43, s[68:69]
	v_cvt_pk_bf16_f32 v40, v35, v40
	v_cndmask_b32_e64 v35, 0, v36, s[58:59]
	v_cndmask_b32_e64 v36, 0, v37, s[70:71]
	v_cndmask_b32_e64 v37, 0, v38, s[72:73]
	v_cndmask_b32_e64 v38, 0, v39, s[74:75]
	ds_write_b64 v108, v[44:45]
	v_cvt_pk_bf16_f32 v44, v48, v50
	v_cvt_pk_bf16_f32 v45, v52, v46
	v_cvt_pk_bf16_f32 v41, v41, v42
	v_cvt_pk_bf16_f32 v36, v35, v36
	v_cvt_pk_bf16_f32 v37, v37, v38
	ds_write_b64 v109, v[44:45]
	ds_write_b64 v110, v[40:41]
	ds_write_b64 v111, v[36:37]
	ds_read_b128 v[36:39], v97 offset:18432
	ds_read_b128 v[40:43], v97 offset:18496
	ds_read_b128 v[44:47], v34 offset:55296
	ds_read_b128 v[48:51], v34 offset:55360
	ds_read_b128 v[52:55], v34 offset:57600
	ds_read_b128 v[56:59], v34 offset:57664
	ds_read_b128 v[60:63], v97 offset:36864
	ds_read_b128 v[64:67], v97 offset:36928
	s_waitcnt lgkmcnt(5)
	v_mfma_f32_16x16x32_bf16 v[78:81], v[36:39], v[44:47], 0
	s_waitcnt lgkmcnt(3)
	v_mfma_f32_16x16x32_bf16 v[36:39], v[36:39], v[52:55], 0
	v_mfma_f32_16x16x32_bf16 v[78:81], v[40:43], v[48:51], v[78:81]
	s_waitcnt lgkmcnt(2)
	v_mfma_f32_16x16x32_bf16 v[36:39], v[40:43], v[56:59], v[36:39]
	s_nop 5
	v_cndmask_b32_e64 v35, v78, 0, s[48:49]
	v_cndmask_b32_e64 v68, 0, v79, s[50:51]
	v_cvt_pk_bf16_f32 v68, v35, v68
	v_cndmask_b32_e64 v35, v36, 0, s[56:57]
	v_cndmask_b32_e64 v40, 0, v37, s[58:59]
	v_cndmask_b32_e64 v41, v38, 0, s[60:61]
	v_cndmask_b32_e64 v42, v39, 0, s[62:63]
	s_waitcnt lgkmcnt(1)
	v_mfma_f32_16x16x32_bf16 v[36:39], v[60:63], v[44:47], 0
	v_cndmask_b32_e64 v69, v80, 0, s[52:53]
	v_cndmask_b32_e64 v78, v81, 0, s[54:55]
	v_cvt_pk_bf16_f32 v69, v69, v78
	s_waitcnt lgkmcnt(0)
	v_mfma_f32_16x16x32_bf16 v[36:39], v[64:67], v[48:51], v[36:39]
	v_cvt_pk_bf16_f32 v40, v35, v40
	v_cvt_pk_bf16_f32 v41, v41, v42
	ds_write_b64 v112, v[68:69]
	ds_write_b64 v113, v[40:41]
	s_nop 3
	v_cndmask_b32_e64 v35, v36, 0, s[48:49]
	v_cndmask_b32_e64 v40, 0, v37, s[50:51]
	v_cndmask_b32_e64 v41, v38, 0, s[52:53]
	v_cndmask_b32_e64 v42, v39, 0, s[54:55]
	v_mfma_f32_16x16x32_bf16 v[36:39], v[60:63], v[52:55], 0
	v_cvt_pk_bf16_f32 v40, v35, v40
	v_cvt_pk_bf16_f32 v41, v41, v42
	ds_write_b64 v114, v[40:41]
	v_mfma_f32_16x16x32_bf16 v[36:39], v[64:67], v[56:59], v[36:39]
	s_nop 7
	v_cndmask_b32_e64 v35, v36, 0, s[56:57]
	v_cndmask_b32_e64 v36, 0, v37, s[58:59]
	v_cndmask_b32_e64 v37, v38, 0, s[60:61]
	v_cndmask_b32_e64 v38, v39, 0, s[62:63]
	v_cvt_pk_bf16_f32 v36, v35, v36
	v_cvt_pk_bf16_f32 v37, v37, v38
	ds_write_b64 v115, v[36:37]
	s_waitcnt lgkmcnt(0)
	s_barrier
; DI void ck_wr_tr(LAS bf16* XT, int m, int n, f32x4 v) { *(LAS u32x2*)(XT + n * CP + m) = (u32x2){pk2(v[0], v[1]), pk2(v[2], v[3])}; }
; #define CK_BAR() do { asm volatile("s_waitcnt lgkmcnt(0)" ::: "memory"); __builtin_amdgcn_s_barrier(); asm volatile("" ::: "memory"); } while (0)
; #define CK_RUN2(A1, B1, E1, A2, B2, E2) do { CkF f1_, f2_; ck_ld(f1_, A1, B1, wave, lane); ck_ld(f2_, A2, B2, wave, lane); __builtin_amdgcn_sched_barrier(0); \
;             f32x4 c1_[2] = CK_Z2, c2_[2] = CK_Z2; ck_mma(c1_, f1_); ck_mma(c2_, f2_); ck_epi(c1_, wave, lane, E1); ck_epi(c2_, wave, lane, E2); } while (0)
; DI void phase_chunkA(const Args& a, LAS unsigned char* lds, int wave, int lane, int tid, int bid, int G) {
;     ...
;         { auto eS1 = [&](int m, int n, f32x4 v) { ck_wr_tr(SL(2), m, n, v); }; auto eS2 = [&](int m, int n, f32x4 v) { ck_wr_tr(SL(0), m, n, v); };
;           CK_RUN2(SL(12), SL(13), eS1, SL(13), SL(12), eS2); }
;         CK_BAR();
;         CK_NEU(8, 4, 0, 2, 12, 13);
;         CK_NEU(4, 8, 12, 13, 0, 2);
;         CK_NEU(8, 4, 0, 2, 12, 13);
;         CK_NEU(4, 8, 12, 13, 0, 2);
	v_add_u32_e32 v37, v118, v98
	ds_read_b128 v[38:41], v117
	ds_read_b128 v[42:45], v117 offset:64
	ds_read_b128 v[46:49], v37
	ds_read_b128 v[50:53], v37 offset:64
	ds_read_b128 v[54:57], v37 offset:2304
	ds_read_b128 v[58:61], v37 offset:2368
	v_add_u32_e32 v35, v116, v98
	ds_read_b128 v[62:65], v119
	ds_read_b128 v[66:69], v119 offset:64
	ds_read_b128 v[78:81], v35
	ds_read_b128 v[82:85], v35 offset:64
	ds_read_b128 v[144:147], v35 offset:2304
	ds_read_b128 v[148:151], v35 offset:2368
	s_waitcnt lgkmcnt(9)
	v_mfma_f32_16x16x32_bf16 v[46:49], v[38:41], v[46:49], 0
	s_waitcnt lgkmcnt(7)
	v_mfma_f32_16x16x32_bf16 v[38:41], v[38:41], v[54:57], 0
	s_waitcnt lgkmcnt(6)
	v_mfma_f32_16x16x32_bf16 v[38:41], v[42:45], v[58:61], v[38:41]
	v_mfma_f32_16x16x32_bf16 v[46:49], v[42:45], v[50:53], v[46:49]
	s_waitcnt lgkmcnt(3)
	v_mfma_f32_16x16x32_bf16 v[42:45], v[62:65], v[78:81], 0
	s_nop 4
	v_cvt_pk_bf16_f32 v38, v38, v39
	v_cvt_pk_bf16_f32 v39, v40, v41
	v_cvt_pk_bf16_f32 v46, v46, v47
	v_cvt_pk_bf16_f32 v47, v48, v49
	ds_write_b64 v99, v[38:39] offset:20736
	s_waitcnt lgkmcnt(3)
	v_mfma_f32_16x16x32_bf16 v[38:41], v[66:69], v[82:85], v[42:45]
	ds_write_b64 v99, v[46:47] offset:18432
	s_waitcnt lgkmcnt(3)
	v_mfma_f32_16x16x32_bf16 v[46:49], v[62:65], v[144:147], 0
	s_nop 4
	v_cvt_pk_bf16_f32 v38, v38, v39
	v_cvt_pk_bf16_f32 v39, v40, v41
	ds_write_b64 v99, v[38:39]
	s_waitcnt lgkmcnt(3)
	v_mfma_f32_16x16x32_bf16 v[38:41], v[66:69], v[148:151], v[46:49]
	s_nop 7
	v_cvt_pk_bf16_f32 v38, v38, v39
	v_cvt_pk_bf16_f32 v39, v40, v41
	ds_write_b64 v99, v[38:39] offset:2304
	s_waitcnt lgkmcnt(0)
	s_barrier
	v_add_u32_e32 v38, v120, v98
	ds_read_b128 v[40:43], v97 offset:18432
	ds_read_b128 v[44:47], v97 offset:18496
	ds_read_b128 v[48:51], v38
	ds_read_b128 v[52:55], v38 offset:64
	ds_read_b128 v[56:59], v38 offset:2304
	ds_read_b128 v[60:63], v38 offset:2368
	ds_read_b128 v[64:67], v97
	ds_read_b128 v[78:81], v97 offset:64
	ds_read_b128 v[82:85], v34 offset:18432
	ds_read_b128 v[144:147], v34 offset:18496
	ds_read_b128 v[148:151], v34 offset:20736
	ds_read_b128 v[152:155], v34 offset:20800
	ds_read_b128 v[156:159], v34
	ds_read_b128 v[160:163], v34 offset:64
	ds_read_b128 v[172:175], v34 offset:2304
	ds_read_b128 v[176:179], v34 offset:2368
	s_waitcnt lgkmcnt(13)
	v_mfma_f32_16x16x32_bf16 v[48:51], v[40:43], v[48:51], 0
	v_add_u32_e32 v36, v106, v98
	s_waitcnt lgkmcnt(11)
	v_mfma_f32_16x16x32_bf16 v[56:59], v[40:43], v[56:59], 0
	v_mfma_f32_16x16x32_bf16 v[48:51], v[44:47], v[52:55], v[48:51]
	s_waitcnt lgkmcnt(10)
	v_mfma_f32_16x16x32_bf16 v[52:55], v[44:47], v[60:63], v[56:59]
	s_waitcnt lgkmcnt(7)
	v_mfma_f32_16x16x32_bf16 v[56:59], v[64:67], v[82:85], 0
	s_waitcnt lgkmcnt(5)
	v_mfma_f32_16x16x32_bf16 v[60:63], v[64:67], v[148:151], 0
	s_waitcnt lgkmcnt(3)
	v_mfma_f32_16x16x32_bf16 v[64:67], v[40:43], v[156:159], 0
	s_waitcnt lgkmcnt(1)
	v_mfma_f32_16x16x32_bf16 v[40:43], v[40:43], v[172:175], 0
	v_mfma_f32_16x16x32_bf16 v[64:67], v[44:47], v[160:163], v[64:67]
	s_waitcnt lgkmcnt(0)
	v_mfma_f32_16x16x32_bf16 v[40:43], v[44:47], v[176:179], v[40:43]
	ds_read_b64 v[44:45], v107
	s_waitcnt lgkmcnt(0)
	v_lshlrev_b32_e32 v46, 16, v44
	v_and_b32_e32 v47, 0xffff0000, v44
	v_lshlrev_b32_e32 v44, 16, v45
	v_and_b32_e32 v45, 0xffff0000, v45
	v_pk_add_f32 v[46:47], v[48:49], v[46:47]
	v_pk_add_f32 v[44:45], v[50:51], v[44:45]
	v_cvt_pk_bf16_f32 v46, v46, v47
	v_cvt_pk_bf16_f32 v47, v44, v45
	ds_read_b64 v[44:45], v36 offset:2304
	v_mfma_f32_16x16x32_bf16 v[56:59], v[78:81], v[144:147], v[56:59]
	ds_write_b64 v121, v[46:47] offset:36864
	v_cvt_pk_bf16_f32 v40, v40, v41
	v_cvt_pk_bf16_f32 v41, v42, v43
	v_mfma_f32_16x16x32_bf16 v[60:63], v[78:81], v[152:155], v[60:63]
	s_waitcnt lgkmcnt(1)
	v_lshlrev_b32_e32 v46, 16, v44
	v_and_b32_e32 v47, 0xffff0000, v44
	v_lshlrev_b32_e32 v44, 16, v45
	v_and_b32_e32 v45, 0xffff0000, v45
	v_pk_add_f32 v[46:47], v[52:53], v[46:47]
	v_pk_add_f32 v[44:45], v[54:55], v[44:45]
	v_cvt_pk_bf16_f32 v46, v46, v47
	v_cvt_pk_bf16_f32 v47, v44, v45
	v_cvt_pk_bf16_f32 v44, v56, v57
	v_cvt_pk_bf16_f32 v45, v58, v59
	ds_write_b64 v121, v[46:47] offset:39168
	ds_write_b64 v122, v[44:45]
	v_cvt_pk_bf16_f32 v44, v60, v61
	v_cvt_pk_bf16_f32 v45, v62, v63
	ds_write_b64 v123, v[44:45]
	v_cvt_pk_bf16_f32 v44, v64, v65
	v_cvt_pk_bf16_f32 v45, v66, v67
	ds_write_b64 v124, v[44:45]
	ds_write_b64 v125, v[40:41]
	s_waitcnt lgkmcnt(0)
	s_barrier
; DI void ck_wr_tr(LAS bf16* XT, int m, int n, f32x4 v) { *(LAS u32x2*)(XT + n * CP + m) = (u32x2){pk2(v[0], v[1]), pk2(v[2], v[3])}; }
; #define CK_BAR() do { asm volatile("s_waitcnt lgkmcnt(0)" ::: "memory"); __builtin_amdgcn_s_barrier(); asm volatile("" ::: "memory"); } while (0)
; #define CK_RUN2(A1, B1, E1, A2, B2, E2) do { CkF f1_, f2_; ck_ld(f1_, A1, B1, wave, lane); ck_ld(f2_, A2, B2, wave, lane); __builtin_amdgcn_sched_barrier(0); \
;             f32x4 c1_[2] = CK_Z2, c2_[2] = CK_Z2; ck_mma(c1_, f1_); ck_mma(c2_, f2_); ck_epi(c1_, wave, lane, E1); ck_epi(c2_, wave, lane, E2); } while (0)
; DI void phase_chunkA(const Args& a, LAS unsigned char* lds, int wave, int lane, int tid, int bid, int G) {
;     ...
;         { auto eS1 = [&](int m, int n, f32x4 v) { ck_wr_tr(SL(2), m, n, v); }; auto eS2 = [&](int m, int n, f32x4 v) { ck_wr_tr(SL(0), m, n, v); };
;           CK_RUN2(SL(12), SL(13), eS1, SL(13), SL(12), eS2); }
;         CK_BAR();
;         CK_NEU(8, 4, 0, 2, 12, 13);
;         CK_NEU(4, 8, 12, 13, 0, 2);
;         CK_NEU(8, 4, 0, 2, 12, 13);
;         CK_NEU(4, 8, 12, 13, 0, 2);
	ds_read_b128 v[40:43], v119
	ds_read_b128 v[44:47], v34 offset:36864
	ds_read_b128 v[48:51], v34 offset:39168
	ds_read_b128 v[52:55], v119 offset:64
	ds_read_b128 v[56:59], v34 offset:36928
	ds_read_b128 v[60:63], v34 offset:39232
	ds_read_b128 v[64:67], v117
	ds_read_b128 v[78:81], v37
	ds_read_b128 v[82:85], v37 offset:2304
	ds_read_b128 v[144:147], v117 offset:64
	ds_read_b128 v[148:151], v37 offset:64
	ds_read_b128 v[152:155], v37 offset:2368
	ds_read_b128 v[156:159], v35
	ds_read_b128 v[160:163], v35 offset:2304
	ds_read_b128 v[172:175], v35 offset:64
	ds_read_b128 v[176:179], v35 offset:2368
	s_waitcnt lgkmcnt(14)
	v_mfma_f32_16x16x32_bf16 v[44:47], v[40:43], v[44:47], 0
	s_waitcnt lgkmcnt(13)
	v_mfma_f32_16x16x32_bf16 v[48:51], v[40:43], v[48:51], 0
	s_waitcnt lgkmcnt(11)
	v_mfma_f32_16x16x32_bf16 v[44:47], v[52:55], v[56:59], v[44:47]
	s_waitcnt lgkmcnt(10)
	v_mfma_f32_16x16x32_bf16 v[48:51], v[52:55], v[60:63], v[48:51]
	s_waitcnt lgkmcnt(8)
	v_mfma_f32_16x16x32_bf16 v[56:59], v[64:67], v[78:81], 0
	s_waitcnt lgkmcnt(7)
	v_mfma_f32_16x16x32_bf16 v[60:63], v[64:67], v[82:85], 0
	s_waitcnt lgkmcnt(3)
	v_mfma_f32_16x16x32_bf16 v[64:67], v[40:43], v[156:159], 0
	s_waitcnt lgkmcnt(2)
	v_mfma_f32_16x16x32_bf16 v[40:43], v[40:43], v[160:163], 0
	s_waitcnt lgkmcnt(1)
	v_mfma_f32_16x16x32_bf16 v[64:67], v[52:55], v[172:175], v[64:67]
	s_waitcnt lgkmcnt(0)
	v_mfma_f32_16x16x32_bf16 v[40:43], v[52:55], v[176:179], v[40:43]
	ds_read_b64 v[52:53], v121 offset:36864
	s_waitcnt lgkmcnt(0)
	v_lshlrev_b32_e32 v54, 16, v52
	v_and_b32_e32 v55, 0xffff0000, v52
	v_lshlrev_b32_e32 v52, 16, v53
	v_and_b32_e32 v53, 0xffff0000, v53
	v_pk_add_f32 v[44:45], v[44:45], v[54:55]
	v_pk_add_f32 v[46:47], v[46:47], v[52:53]
	v_cvt_pk_bf16_f32 v44, v44, v45
	v_cvt_pk_bf16_f32 v45, v46, v47
	ds_write_b64 v107, v[44:45]
	ds_read_b64 v[44:45], v121 offset:39168
	v_mfma_f32_16x16x32_bf16 v[56:59], v[144:147], v[148:151], v[56:59]
	v_cvt_pk_bf16_f32 v40, v40, v41
	v_cvt_pk_bf16_f32 v41, v42, v43
	s_waitcnt lgkmcnt(0)
	v_lshlrev_b32_e32 v46, 16, v44
	v_mfma_f32_16x16x32_bf16 v[60:63], v[144:147], v[152:155], v[60:63]
	v_and_b32_e32 v47, 0xffff0000, v44
	v_lshlrev_b32_e32 v44, 16, v45
	v_and_b32_e32 v45, 0xffff0000, v45
	v_pk_add_f32 v[46:47], v[48:49], v[46:47]
	v_pk_add_f32 v[44:45], v[50:51], v[44:45]
	v_cvt_pk_bf16_f32 v46, v46, v47
	v_cvt_pk_bf16_f32 v47, v44, v45
	v_cvt_pk_bf16_f32 v44, v56, v57
	v_cvt_pk_bf16_f32 v45, v58, v59
	ds_write_b64 v36, v[46:47] offset:2304
	ds_write_b64 v99, v[44:45] offset:18432
	v_cvt_pk_bf16_f32 v44, v60, v61
	v_cvt_pk_bf16_f32 v45, v62, v63
	ds_write_b64 v99, v[44:45] offset:20736
	v_cvt_pk_bf16_f32 v44, v64, v65
	v_cvt_pk_bf16_f32 v45, v66, v67
	ds_write_b64 v99, v[44:45]
	ds_write_b64 v99, v[40:41] offset:2304
	s_waitcnt lgkmcnt(0)
	s_barrier
	ds_read_b128 v[40:43], v97 offset:18432
	ds_read_b128 v[44:47], v38
	ds_read_b128 v[48:51], v38 offset:2304
	ds_read_b128 v[52:55], v97 offset:18496
	ds_read_b128 v[56:59], v38 offset:64
	ds_read_b128 v[60:63], v38 offset:2368
	ds_read_b128 v[64:67], v97
	ds_read_b128 v[78:81], v34 offset:18432
	ds_read_b128 v[82:85], v34 offset:20736
	ds_read_b128 v[144:147], v97 offset:64
	ds_read_b128 v[148:151], v34 offset:18496
	ds_read_b128 v[152:155], v34 offset:20800
	ds_read_b128 v[156:159], v34
	ds_read_b128 v[160:163], v34 offset:2304
	ds_read_b128 v[172:175], v34 offset:64
	ds_read_b128 v[176:179], v34 offset:2368
	s_waitcnt lgkmcnt(14)
	v_mfma_f32_16x16x32_bf16 v[44:47], v[40:43], v[44:47], 0
	s_waitcnt lgkmcnt(13)
	v_mfma_f32_16x16x32_bf16 v[48:51], v[40:43], v[48:51], 0
	s_waitcnt lgkmcnt(11)
	v_mfma_f32_16x16x32_bf16 v[44:47], v[52:55], v[56:59], v[44:47]
	s_waitcnt lgkmcnt(10)
	v_mfma_f32_16x16x32_bf16 v[48:51], v[52:55], v[60:63], v[48:51]
	s_waitcnt lgkmcnt(8)
	v_mfma_f32_16x16x32_bf16 v[56:59], v[64:67], v[78:81], 0
	s_waitcnt lgkmcnt(7)
	v_mfma_f32_16x16x32_bf16 v[60:63], v[64:67], v[82:85], 0
	s_waitcnt lgkmcnt(3)
	v_mfma_f32_16x16x32_bf16 v[64:67], v[40:43], v[156:159], 0
	s_waitcnt lgkmcnt(2)
	v_mfma_f32_16x16x32_bf16 v[38:41], v[40:43], v[160:163], 0
	ds_read_b64 v[42:43], v107
	s_waitcnt lgkmcnt(2)
	v_mfma_f32_16x16x32_bf16 v[64:67], v[52:55], v[172:175], v[64:67]
	s_waitcnt lgkmcnt(1)
	v_mfma_f32_16x16x32_bf16 v[38:41], v[52:55], v[176:179], v[38:41]
	s_waitcnt lgkmcnt(0)
	v_lshlrev_b32_e32 v52, 16, v42
	v_and_b32_e32 v53, 0xffff0000, v42
	v_lshlrev_b32_e32 v42, 16, v43
	v_and_b32_e32 v43, 0xffff0000, v43
	v_pk_add_f32 v[44:45], v[44:45], v[52:53]
	v_pk_add_f32 v[42:43], v[46:47], v[42:43]
	v_cvt_pk_bf16_f32 v44, v44, v45
	v_cvt_pk_bf16_f32 v45, v42, v43
	ds_read_b64 v[42:43], v36 offset:2304
	v_mfma_f32_16x16x32_bf16 v[56:59], v[144:147], v[148:151], v[56:59]
	ds_write_b64 v121, v[44:45] offset:36864
	v_cvt_pk_bf16_f32 v38, v38, v39
	v_cvt_pk_bf16_f32 v39, v40, v41
	v_mfma_f32_16x16x32_bf16 v[60:63], v[144:147], v[152:155], v[60:63]
	s_waitcnt lgkmcnt(1)
	v_lshlrev_b32_e32 v44, 16, v42
	v_and_b32_e32 v45, 0xffff0000, v42
	v_lshlrev_b32_e32 v42, 16, v43
	v_and_b32_e32 v43, 0xffff0000, v43
	v_pk_add_f32 v[44:45], v[48:49], v[44:45]
	v_pk_add_f32 v[42:43], v[50:51], v[42:43]
	v_cvt_pk_bf16_f32 v44, v44, v45
	v_cvt_pk_bf16_f32 v45, v42, v43
	v_cvt_pk_bf16_f32 v42, v56, v57
	v_cvt_pk_bf16_f32 v43, v58, v59
	ds_write_b64 v121, v[44:45] offset:39168
	ds_write_b64 v122, v[42:43]
	v_cvt_pk_bf16_f32 v42, v60, v61
	v_cvt_pk_bf16_f32 v43, v62, v63
	ds_write_b64 v123, v[42:43]
	v_cvt_pk_bf16_f32 v42, v64, v65
	v_cvt_pk_bf16_f32 v43, v66, v67
	ds_write_b64 v124, v[42:43]
	ds_write_b64 v125, v[38:39]
	s_waitcnt lgkmcnt(0)
	s_barrier
; #define LAS __attribute__((address_space(3)))
; DI void ck_wr_tr(LAS bf16* XT, int m, int n, f32x4 v) { *(LAS u32x2*)(XT + n * CP + m) = (u32x2){pk2(v[0], v[1]), pk2(v[2], v[3])}; }
; #define CK_BAR() do { asm volatile("s_waitcnt lgkmcnt(0)" ::: "memory"); __builtin_amdgcn_s_barrier(); asm volatile("" ::: "memory"); } while (0)
; #define CK_RUN2(A1, B1, E1, A2, B2, E2) do { CkF f1_, f2_; ck_ld(f1_, A1, B1, wave, lane); ck_ld(f2_, A2, B2, wave, lane); __builtin_amdgcn_sched_barrier(0); \
;             f32x4 c1_[2] = CK_Z2, c2_[2] = CK_Z2; ck_mma(c1_, f1_); ck_mma(c2_, f2_); ck_epi(c1_, wave, lane, E1); ck_epi(c2_, wave, lane, E2); } while (0)
; DI void phase_chunkA(const Args& a, LAS unsigned char* lds, int wave, int lane, int tid, int bid, int G) {
;     ...
;         CK_NEU(4, 8, 12, 13, 0, 2);
;         CK_NEU(8, 4, 0, 2, 12, 13);
;         CK_NEU(4, 8, 12, 13, 0, 2);
;         ck_mm(SL(2), SL(8), nullptr, nullptr, wave, lane, [&](int m, int n, f32x4 v) { const u32x2 o = *(const LAS u32x2*)(SL(8) + n * CP + m);
;             v[0] += bflo(o.x); v[1] += bfhi(o.x); v[2] += bflo(o.y); v[3] += bfhi(o.y); ck_wr_tr(SL(4), m, n, v); });
;         CK_BAR();
;     ...
;         { auto e12 = [&](int m, int n, f32x4 v) { ck_wr_tr(SL(12), m, n, v); }; auto e0 = [&](int m, int n, f32x4 v) { ck_wr_tr(SL(0), m, n, v); };
;           CK_RUN2(SL(9), SL(7), e12, SL(4), SL(1), e0); }
;         CK_BAR();
	ds_read_b128 v[38:41], v119
	ds_read_b128 v[42:45], v34 offset:36864
	ds_read_b128 v[46:49], v34 offset:39168
	ds_read_b128 v[50:53], v119 offset:64
	ds_read_b128 v[54:57], v34 offset:36928
	ds_read_b128 v[58:61], v34 offset:39232
	ds_read_b128 v[62:65], v117
	ds_read_b128 v[66:69], v37
	ds_read_b128 v[78:81], v37 offset:2304
	ds_read_b128 v[82:85], v117 offset:64
	ds_read_b128 v[144:147], v37 offset:64
	ds_read_b128 v[148:151], v37 offset:2368
	ds_read_b128 v[152:155], v35
	ds_read_b128 v[156:159], v35 offset:2304
	ds_read_b128 v[160:163], v35 offset:64
	ds_read_b128 v[172:175], v35 offset:2368
	s_waitcnt lgkmcnt(14)
	v_mfma_f32_16x16x32_bf16 v[42:45], v[38:41], v[42:45], 0
	s_waitcnt lgkmcnt(13)
	v_mfma_f32_16x16x32_bf16 v[46:49], v[38:41], v[46:49], 0
	s_waitcnt lgkmcnt(11)
	v_mfma_f32_16x16x32_bf16 v[42:45], v[50:53], v[54:57], v[42:45]
	s_waitcnt lgkmcnt(10)
	v_mfma_f32_16x16x32_bf16 v[46:49], v[50:53], v[58:61], v[46:49]
	s_waitcnt lgkmcnt(8)
	v_mfma_f32_16x16x32_bf16 v[54:57], v[62:65], v[66:69], 0
	s_waitcnt lgkmcnt(7)
	v_mfma_f32_16x16x32_bf16 v[58:61], v[62:65], v[78:81], 0
	s_waitcnt lgkmcnt(3)
	v_mfma_f32_16x16x32_bf16 v[62:65], v[38:41], v[152:155], 0
	s_waitcnt lgkmcnt(2)
	v_mfma_f32_16x16x32_bf16 v[38:41], v[38:41], v[156:159], 0
	s_waitcnt lgkmcnt(1)
	v_mfma_f32_16x16x32_bf16 v[62:65], v[50:53], v[160:163], v[62:65]
	s_waitcnt lgkmcnt(0)
	v_mfma_f32_16x16x32_bf16 v[38:41], v[50:53], v[172:175], v[38:41]
	ds_read_b64 v[50:51], v121 offset:36864
	s_waitcnt lgkmcnt(0)
	v_lshlrev_b32_e32 v52, 16, v50
	v_and_b32_e32 v53, 0xffff0000, v50
	v_lshlrev_b32_e32 v50, 16, v51
	v_and_b32_e32 v51, 0xffff0000, v51
	v_pk_add_f32 v[42:43], v[42:43], v[52:53]
	v_pk_add_f32 v[44:45], v[44:45], v[50:51]
	v_cvt_pk_bf16_f32 v42, v42, v43
	v_cvt_pk_bf16_f32 v43, v44, v45
	ds_write_b64 v107, v[42:43]
	ds_read_b64 v[42:43], v121 offset:39168
	v_mfma_f32_16x16x32_bf16 v[54:57], v[82:85], v[144:147], v[54:57]
	s_waitcnt lgkmcnt(0)
	v_lshlrev_b32_e32 v44, 16, v42
	v_mfma_f32_16x16x32_bf16 v[58:61], v[82:85], v[148:151], v[58:61]
	v_and_b32_e32 v45, 0xffff0000, v42
	v_lshlrev_b32_e32 v42, 16, v43
	v_and_b32_e32 v43, 0xffff0000, v43
	v_pk_add_f32 v[44:45], v[46:47], v[44:45]
	v_pk_add_f32 v[42:43], v[48:49], v[42:43]
	v_cvt_pk_bf16_f32 v44, v44, v45
	v_cvt_pk_bf16_f32 v45, v42, v43
	ds_write_b64 v36, v[44:45] offset:2304
	v_cvt_pk_bf16_f32 v36, v54, v55
	v_cvt_pk_bf16_f32 v37, v56, v57
	ds_write_b64 v99, v[36:37] offset:18432
	v_cvt_pk_bf16_f32 v36, v58, v59
	v_cvt_pk_bf16_f32 v37, v60, v61
	ds_write_b64 v99, v[36:37] offset:20736
	v_cvt_pk_bf16_f32 v36, v62, v63
	v_cvt_pk_bf16_f32 v37, v64, v65
	ds_write_b64 v99, v[36:37]
	v_cvt_pk_bf16_f32 v36, v38, v39
	v_cvt_pk_bf16_f32 v37, v40, v41
	ds_write_b64 v99, v[36:37] offset:2304
	s_waitcnt lgkmcnt(0)
	s_barrier
	ds_read_b128 v[36:39], v97 offset:18432
	v_add_u32_e32 v56, v120, v126
	ds_read_b128 v[40:43], v56
	ds_read_b128 v[44:47], v56 offset:2304
	ds_read_b128 v[48:51], v97 offset:18496
	ds_read_b128 v[52:55], v56 offset:64
	ds_read_b128 v[56:59], v56 offset:2368
	s_waitcnt lgkmcnt(4)
	v_mfma_f32_16x16x32_bf16 v[40:43], v[36:39], v[40:43], 0
	s_waitcnt lgkmcnt(3)
	v_mfma_f32_16x16x32_bf16 v[36:39], v[36:39], v[44:47], 0
	ds_read_b64 v[44:45], v127
	s_waitcnt lgkmcnt(0)
	v_lshlrev_b32_e32 v46, 16, v44
	v_mfma_f32_16x16x32_bf16 v[40:43], v[48:51], v[52:55], v[40:43]
	v_and_b32_e32 v47, 0xffff0000, v44
	v_lshlrev_b32_e32 v44, 16, v45
	v_and_b32_e32 v45, 0xffff0000, v45
	v_mfma_f32_16x16x32_bf16 v[36:39], v[48:51], v[56:59], v[36:39]
	s_nop 3
	v_add_f32_e64 v40, v40, v46
	v_add_f32_e64 v41, v41, v47
	v_pk_add_f32 v[42:43], v[42:43], v[44:45]
	v_cvt_pk_bf16_f32 v40, v40, v41
	v_cvt_pk_bf16_f32 v41, v42, v43
	ds_write_b64 v128, v[40:41] offset:36864
	v_add_u32_e32 v40, v106, v126
	ds_read_b64 v[40:41], v40 offset:2304
	s_waitcnt lgkmcnt(0)
	v_lshlrev_b32_e32 v42, 16, v40
	v_and_b32_e32 v43, 0xffff0000, v40
	v_lshlrev_b32_e32 v40, 16, v41
	v_and_b32_e32 v41, 0xffff0000, v41
	v_pk_add_f32 v[36:37], v[36:37], v[42:43]
	v_pk_add_f32 v[38:39], v[38:39], v[40:41]
	v_cvt_pk_bf16_f32 v36, v36, v37
	v_cvt_pk_bf16_f32 v37, v38, v39
	ds_write_b64 v128, v[36:37] offset:39168
	s_waitcnt lgkmcnt(0)
	s_barrier
	ds_read_b128 v[36:39], v129
	ds_read_b128 v[40:43], v34 offset:64512
	ds_read_b128 v[44:47], v143 offset:64512
	ds_read_b128 v[48:51], v129 offset:64
	ds_read_b128 v[52:55], v34 offset:64576
	ds_read_b128 v[56:59], v143 offset:64576
	ds_read_b128 v[60:63], v97 offset:36864
	ds_read_b128 v[64:67], v34 offset:9216
	ds_read_b128 v[78:81], v34 offset:11520
	ds_read_b128 v[82:85], v97 offset:36928
	ds_read_b128 v[144:147], v34 offset:9280
	ds_read_b128 v[148:151], v34 offset:11584
	s_waitcnt lgkmcnt(10)
	v_mfma_f32_16x16x32_bf16 v[40:43], v[36:39], v[40:43], 0
	s_ashr_i32 s29, s28, 31
	s_lshl_b64 s[26:27], s[28:29], 13
	s_add_u32 s2, s5, s26
	s_waitcnt lgkmcnt(9)
	v_mfma_f32_16x16x32_bf16 v[36:39], v[36:39], v[44:47], 0
	s_addc_u32 s3, s7, s27
	s_add_u32 vcc_lo, s0, s26
	s_addc_u32 vcc_hi, s33, s27
	s_waitcnt lgkmcnt(6)
	v_mfma_f32_16x16x32_bf16 v[36:39], v[48:51], v[56:59], v[36:39]
	v_mfma_f32_16x16x32_bf16 v[40:43], v[48:51], v[52:55], v[40:43]
	s_waitcnt lgkmcnt(4)
	v_mfma_f32_16x16x32_bf16 v[44:47], v[60:63], v[64:67], 0
	s_nop 4
	v_cvt_pk_bf16_f32 v36, v36, v37
	v_cvt_pk_bf16_f32 v37, v38, v39
	v_cvt_pk_bf16_f32 v40, v40, v41
	v_cvt_pk_bf16_f32 v41, v42, v43
	ds_write_b64 v125, v[36:37]
	s_waitcnt lgkmcnt(2)
	v_mfma_f32_16x16x32_bf16 v[36:39], v[82:85], v[144:147], v[44:47]
	ds_write_b64 v124, v[40:41]
	v_mfma_f32_16x16x32_bf16 v[40:43], v[60:63], v[78:81], 0
	s_nop 5
	v_cvt_pk_bf16_f32 v36, v36, v37
	v_cvt_pk_bf16_f32 v37, v38, v39
	ds_write_b64 v99, v[36:37]
	s_waitcnt lgkmcnt(3)
	v_mfma_f32_16x16x32_bf16 v[36:39], v[82:85], v[148:151], v[40:43]
	s_nop 7
	v_cvt_pk_bf16_f32 v36, v36, v37
	v_cvt_pk_bf16_f32 v37, v38, v39
	ds_write_b64 v99, v[36:37] offset:2304
	s_waitcnt lgkmcnt(0)
	s_barrier
; #define LAS __attribute__((address_space(3)))
; DI unsigned pk2(float a, float b) { f32x2 v = {a, b}; bf16x2_t r = __builtin_convertvector(v, bf16x2_t); return __builtin_bit_cast(unsigned, r); }
; DI void ck_wr_tr(LAS bf16* XT, int m, int n, f32x4 v) { *(LAS u32x2*)(XT + n * CP + m) = (u32x2){pk2(v[0], v[1]), pk2(v[2], v[3])}; }
; DI void phase_chunkA(const Args& a, LAS unsigned char* lds, int wave, int lane, int tid, int bid, int G) {
;     ...
;         { bf16* Pg = (bf16*)(ws + CH_P) + (size_t)cid * 4096; bf16* Rg = (bf16*)(ws + CH_RH) + (size_t)cid * 4096;
;           auto e13 = [&](int m, int n, f32x4 v) { ck_wr_tr(SL(13), m, n, v); };
;           auto eP = [&](int m, int n, f32x4 v) { const float gc = gC[n];
; #pragma unroll
;               for (int g = 0; g < 4; ++g) v[g] = gc * (((m + g == n) ? 1.f : 0.f) + v[g]);
;               *(u32x2*)(Pg + n * 64 + m) = (u32x2){pk2(v[0], v[1]), pk2(v[2], v[3])}; };
;           auto eR = [&](int m, int n, f32x4 v) { const u32x2 o = *(const LAS u32x2*)(SL(6) + n * CP + m);
;               v[0] += bflo(o.x); v[1] += bfhi(o.x); v[2] += bflo(o.y); v[3] += bfhi(o.y);
;               *(u32x2*)(Rg + n * 64 + m) = (u32x2){pk2(v[0], v[1]), pk2(v[2], v[3])}; };
;           CK_RUN3(SL(4), SL(12), e13, SL(0), SL(3), eP, SL(0), SL(10), eR); }
	ds_read_b128 v[36:39], v97 offset:36864
	ds_read_b128 v[40:43], v97 offset:36928
	ds_read_b128 v[44:47], v35
	ds_read_b128 v[48:51], v35 offset:64
	ds_read_b128 v[52:55], v35 offset:2304
	ds_read_b128 v[56:59], v35 offset:2368
	ds_read_b128 v[60:63], v97
	ds_read_b128 v[64:67], v97 offset:64
	ds_read_b128 v[78:81], v34 offset:27648
	ds_read_b128 v[82:85], v34 offset:27712
	ds_read_b128 v[144:147], v34 offset:29952
	ds_read_b128 v[148:151], v34 offset:30016
	v_add_u32_e32 v35, v100, v98
	ds_read_b128 v[152:155], v35
	ds_read_b128 v[156:159], v35 offset:64
	ds_read_b128 v[160:163], v35 offset:2304
	ds_read_b128 v[172:175], v35 offset:2368
	s_waitcnt lgkmcnt(13)
	v_mfma_f32_16x16x32_bf16 v[44:47], v[36:39], v[44:47], 0
	v_lshlrev_b32_e32 v90, 1, v72
	s_waitcnt lgkmcnt(11)
	v_mfma_f32_16x16x32_bf16 v[36:39], v[36:39], v[52:55], 0
	v_lshlrev_b64 v[52:53], 1, v[70:71]
	v_and_b32_e32 v240, 12, v70
	v_lshlrev_b32_e32 v240, 1, v240
	v_and_b32_e32 v241, 32, v70
	v_or_b32_e32 v240, v240, v241
	v_bfe_u32 v241, v70, 4, 1
	v_lshl_or_b32 v240, v241, 2, v240
	v_lshlrev_b32_e32 v240, 1, v240
	v_mov_b32_e32 v241, 0
	v_mfma_f32_16x16x32_bf16 v[44:47], v[40:43], v[48:51], v[44:47]
	s_waitcnt lgkmcnt(10)
	v_mfma_f32_16x16x32_bf16 v[36:39], v[40:43], v[56:59], v[36:39]
	s_waitcnt lgkmcnt(7)
	v_mfma_f32_16x16x32_bf16 v[40:43], v[60:63], v[78:81], 0
	s_nop 3
	v_cvt_pk_bf16_f32 v44, v44, v45
	v_cvt_pk_bf16_f32 v45, v46, v47
	v_cvt_pk_bf16_f32 v36, v36, v37
	v_cvt_pk_bf16_f32 v37, v38, v39
	ds_write_b64 v122, v[44:45]
	ds_write_b64 v123, v[36:37]
	ds_read_b32 v44, v130
	s_waitcnt lgkmcnt(9)
	v_mfma_f32_16x16x32_bf16 v[36:39], v[64:67], v[82:85], v[40:43]
	ds_read_b32 v54, v135
	ds_read_b64 v[48:49], v140 offset:55296
	ds_read_b64 v[50:51], v121 offset:55296
	v_lshl_add_u64 v[42:43], s[2:3], 0, v[90:91]
	v_lshl_add_u64 v[42:43], v[42:43], 0, v[240:241]
	s_nop 2
	v_add_f32_e32 v36, v131, v36
	v_add_f32_e32 v37, v132, v37
	v_add_f32_e32 v38, v133, v38
	v_add_f32_e32 v39, v134, v39
	s_waitcnt lgkmcnt(3)
	v_mul_f32_e32 v36, v36, v44
	v_mul_f32_e32 v37, v37, v44
	v_mul_f32_e32 v38, v38, v44
	v_mul_f32_e32 v39, v39, v44
	v_cvt_pk_bf16_f32 v40, v36, v37
	v_cvt_pk_bf16_f32 v41, v38, v39
	v_mfma_f32_16x16x32_bf16 v[36:39], v[60:63], v[144:147], 0
	global_store_dwordx2 v[42:43], v[40:41], off
	v_mfma_f32_16x16x32_bf16 v[36:39], v[64:67], v[148:151], v[36:39]
	v_mfma_f32_16x16x32_bf16 v[40:43], v[60:63], v[152:155], 0
	v_mfma_f32_16x16x32_bf16 v[44:47], v[60:63], v[160:163], 0
	s_nop 5
	v_add_f32_e32 v36, v136, v36
	s_waitcnt lgkmcnt(2)
	v_mul_f32_e32 v55, v36, v54
	v_add_f32_e32 v36, v137, v37
	v_mul_f32_e32 v56, v36, v54
	v_add_f32_e32 v36, v138, v38
	v_add_f32_e32 v58, v139, v39
	v_mul_f32_e32 v57, v36, v54
	v_mfma_f32_16x16x32_bf16 v[36:39], v[64:67], v[156:159], v[40:43]
	s_nop 2
	v_mul_f32_e32 v40, v58, v54
	v_cvt_pk_bf16_f32 v54, v55, v56
	v_cvt_pk_bf16_f32 v55, v57, v40
	v_mfma_f32_16x16x32_bf16 v[40:43], v[64:67], v[172:175], v[44:47]
	s_nop 2
	v_lshlrev_b32_e32 v44, 1, v74
	v_mov_b32_e32 v45, v91
	v_lshl_add_u64 v[46:47], s[2:3], 0, v[44:45]
	v_lshl_add_u64 v[46:47], v[46:47], 0, v[240:241]
	global_store_dwordx2 v[46:47], v[54:55], off
	s_waitcnt lgkmcnt(0)
	v_lshlrev_b32_e32 v46, 16, v50
	v_and_b32_e32 v47, 0xffff0000, v50
	v_pk_add_f32 v[36:37], v[36:37], v[46:47]
	v_lshlrev_b32_e32 v46, 16, v51
	v_and_b32_e32 v47, 0xffff0000, v51
	v_pk_add_f32 v[38:39], v[38:39], v[46:47]
	v_cvt_pk_bf16_f32 v36, v36, v37
	v_cvt_pk_bf16_f32 v37, v38, v39
	v_lshl_add_u64 v[38:39], vcc, 0, v[90:91]
	v_lshl_add_u64 v[38:39], v[38:39], 0, v[52:53]
	global_store_dwordx2 v[38:39], v[36:37], off
	v_lshlrev_b32_e32 v36, 16, v48
	v_and_b32_e32 v37, 0xffff0000, v48
	v_lshlrev_b32_e32 v38, 16, v49
	v_and_b32_e32 v39, 0xffff0000, v49
	v_pk_add_f32 v[36:37], v[40:41], v[36:37]
	v_pk_add_f32 v[38:39], v[42:43], v[38:39]
	v_cvt_pk_bf16_f32 v36, v36, v37
	v_cvt_pk_bf16_f32 v37, v38, v39
	v_lshl_add_u64 v[38:39], vcc, 0, v[44:45]
	v_lshl_add_u64 v[38:39], v[38:39], 0, v[52:53]
	global_store_dwordx2 v[38:39], v[36:37], off
	s_waitcnt lgkmcnt(0)
	s_barrier
; DI void phase_chunkA(const Args& a, LAS unsigned char* lds, int wave, int lane, int tid, int bid, int G) {
;     ...
;         { float* Qg = (float*)(ws + CH_Q) + (size_t)cid * 4096; float* Yg = (float*)(ws + CH_YL) + (size_t)cid * 4096;
;           CkF f1, f2, f3, f4; ck_ld(f1, SL(13), SL(3), wave, lane); ck_ld(f2, SL(7), SL(5), wave, lane); ck_ld(f3, SL(13), SL(10), wave, lane); ck_ld(f4, SL(7), SL(11), wave, lane); __builtin_amdgcn_sched_barrier(0);
;           f32x4 cq[2] = CK_Z2, cy[2] = CK_Z2; ck_mma(cq, f1); ck_mma(cq, f2); ck_mma(cy, f3); ck_mma(cy, f4);
;           ck_epi(cq, wave, lane, [&](int m, int n, f32x4 v) { *(f32x4*)(Qg + n * 64 + m) = v * gC[n]; });
;           ck_epi(cy, wave, lane, [&](int m, int n, f32x4 v) { *(f32x4*)(Yg + n * 64 + m) = v; }); }
	ds_read_b128 v[36:39], v119
	ds_read_b128 v[40:43], v119 offset:64
	ds_read_b128 v[44:47], v34 offset:27648
	ds_read_b128 v[48:51], v34 offset:27712
	ds_read_b128 v[52:55], v34 offset:29952
	ds_read_b128 v[56:59], v34 offset:30016
	ds_read_b128 v[60:63], v97 offset:64512
	ds_read_b128 v[64:67], v97 offset:64576
	ds_read_b128 v[78:81], v34 offset:46080
	ds_read_b128 v[82:85], v34 offset:46144
	ds_read_b128 v[144:147], v34 offset:48384
	ds_read_b128 v[148:151], v34 offset:48448
	ds_read_b128 v[152:155], v35
	ds_read_b128 v[156:159], v35 offset:64
	ds_read_b128 v[160:163], v35 offset:2304
	ds_read_b128 v[172:175], v35 offset:2368
	ds_read_b128 v[176:179], v142
	ds_read_b128 v[180:183], v142 offset:64
	ds_read_b128 v[184:187], v142 offset:2304
	ds_read_b128 v[188:191], v142 offset:2368
	s_lshl_b64 s[2:3], s[28:29], 14
	s_add_u32 s26, s1, s2
	s_addc_u32 s27, s24, s3
	s_waitcnt lgkmcnt(14)
	v_mfma_f32_16x16x32_bf16 v[44:47], v[36:39], v[44:47], 0
	v_lshlrev_b32_e32 v90, 2, v72
	s_mov_b32 s28, s25
	v_mfma_f32_16x16x32_bf16 v[44:47], v[40:43], v[48:51], v[44:47]
	v_mfma_f32_16x16x32_bf16 v[52:55], v[36:39], v[52:55], 0
	s_waitcnt lgkmcnt(11)
	v_mfma_f32_16x16x32_bf16 v[44:47], v[60:63], v[78:81], v[44:47]
	v_mfma_f32_16x16x32_bf16 v[48:51], v[40:43], v[56:59], v[52:55]
	ds_read_b32 v34, v130
	ds_read_b32 v56, v135
	v_lshlrev_b64 v[58:59], 2, v[70:71]
	s_waitcnt lgkmcnt(12)
	v_mfma_f32_16x16x32_bf16 v[44:47], v[64:67], v[82:85], v[44:47]
	s_waitcnt lgkmcnt(9)
	v_mfma_f32_16x16x32_bf16 v[52:55], v[36:39], v[152:155], 0
	s_waitcnt lgkmcnt(8)
	v_mfma_f32_16x16x32_bf16 v[52:55], v[40:43], v[156:159], v[52:55]
	s_waitcnt lgkmcnt(1)
	s_nop 2
	v_pk_mul_f32 v[46:47], v[46:47], v[34:35] op_sel_hi:[1,0]
	v_pk_mul_f32 v[44:45], v[44:45], v[34:35] op_sel_hi:[1,0]
	v_mfma_f32_16x16x32_bf16 v[34:37], v[36:39], v[160:163], 0
	v_lshl_add_u64 v[38:39], s[26:27], 0, v[90:91]
	v_lshl_add_u64 v[38:39], v[38:39], 0, v[58:59]
	v_lshlrev_b32_e32 v90, 2, v74
	v_mfma_f32_16x16x32_bf16 v[48:51], v[60:63], v[144:147], v[48:51]
	global_store_dwordx4 v[38:39], v[44:47], off
	v_lshl_add_u64 v[38:39], s[26:27], 0, v[90:91]
	v_mfma_f32_16x16x32_bf16 v[34:37], v[40:43], v[172:175], v[34:37]
	v_lshl_add_u64 v[42:43], v[38:39], 0, v[58:59]
	v_mfma_f32_16x16x32_bf16 v[38:41], v[60:63], v[176:179], v[52:55]
	v_mfma_f32_16x16x32_bf16 v[48:51], v[64:67], v[148:151], v[48:51]
	s_waitcnt vmcnt(5)
	s_nop 0
	v_mov_b32_e32 v52, v32
	v_mov_b32_e32 v53, v33
	v_mfma_f32_16x16x32_bf16 v[34:37], v[60:63], v[184:187], v[34:37]
	v_mfma_f32_16x16x32_bf16 v[38:41], v[64:67], v[180:183], v[38:41]
	s_waitcnt lgkmcnt(0)
	s_nop 0
	v_pk_mul_f32 v[46:47], v[50:51], v[56:57] op_sel_hi:[1,0]
	v_pk_mul_f32 v[44:45], v[48:49], v[56:57] op_sel_hi:[1,0]
	global_store_dwordx4 v[42:43], v[44:47], off
	v_lshl_add_u64 v[42:43], v[76:77], 0, s[2:3]
	v_mfma_f32_16x16x32_bf16 v[34:37], v[64:67], v[188:191], v[34:37]
	v_lshl_add_u64 v[42:43], v[42:43], 0, v[58:59]
	global_store_dwordx4 v[42:43], v[38:41], off
	v_mov_b64_e32 v[60:61], v[12:13]
	v_mov_b64_e32 v[56:57], v[8:9]
	v_add_co_u32_e32 v38, vcc, 0x1000, v42
	v_mov_b64_e32 v[48:49], v[28:29]
	s_nop 0
	v_addc_co_u32_e32 v39, vcc, 0, v43, vcc
	global_store_dwordx4 v[38:39], v[34:37], off
	v_mov_b64_e32 v[40:41], v[20:21]
	v_mov_b64_e32 v[44:45], v[24:25]
	v_mov_b64_e32 v[36:37], v[16:17]
	s_andn2_b64 vcc, exec, s[96:97]
	v_mov_b64_e32 v[58:59], v[10:11]
	v_mov_b64_e32 v[54:55], v[6:7]
	v_mov_b64_e32 v[34:35], v[14:15]
	v_mov_b64_e32 v[38:39], v[18:19]
	v_mov_b64_e32 v[42:43], v[22:23]
	v_mov_b64_e32 v[46:47], v[26:27]
	v_mov_b32_e32 v50, v30
	v_mov_b32_e32 v51, v31
	s_cbranch_vccz .LBB0_1041

; #define LAS __attribute__((address_space(3)))
; DI void phase_chunkB(const Args& a, LAS unsigned char* lds, int wave, int lane, int bid, int G) {
;     ...
;     for (int u = bid; u < NB * NH * 4; u += G) { const int iq = u & 3, bh = u >> 2;
;         bf16x8 pf[3][4][2]; f32x4 qv[3][4];
;     ...
;         asm volatile("s_waitcnt lgkmcnt(0)" ::: "memory");
; #pragma unroll
;         for (int mt = 0; mt < 4; ++mt) { *(LAS u32x2*)(Zb + r * CP + 16 * mt + 4 * q) = (u32x2){0u, 0u};
;             *(u32x2*)((bf16*)(ws + CH_ZS) + ((size_t)bh * NCK) * 4096 + (16 * iq + r) * 64 + 16 * mt + 4 * q) = (u32x2){0u, 0u}; }
;         CB_LOAD(0, 0); CB_LOAD(1, 1); CB_LOAD(2, 2);
.LBB0_1147:
	s_and_b32 s24, s28, 3
	s_ashr_i32 s33, s29, 2
	s_lshl_b32 s25, s24, 4
	s_and_b32 s36, s29, 3
	s_mul_i32 s31, s33, 0x42000
	v_lshl_or_b32 v148, s24, 11, v178
	s_mul_hi_i32 s30, s33, 0x42000
	s_add_u32 s24, s3, s31
	v_add_lshl_u32 v90, v237, s25, 2
	v_add_lshl_u32 v150, v238, s25, 2
	v_add_lshl_u32 v152, v239, s25, 2
	v_add_lshl_u32 v154, v240, s25, 2
	v_add_lshl_u32 v156, v241, s25, 2
	v_add_lshl_u32 v158, v242, s25, 2
	v_add_lshl_u32 v160, v243, s25, 2
	v_add_lshl_u32 v162, v244, s25, 2
	v_add_u32_e32 v204, s25, v245
	v_add_u32_e32 v206, s25, v246
	v_add_u32_e32 v208, s25, v247
	v_add_u32_e32 v210, s25, v248
	v_add_u32_e32 v212, s25, v236
	s_addc_u32 s25, s4, s30
	s_waitcnt vmcnt(31)
	v_lshl_or_b32 v2, s36, 11, v178
	v_mov_b32_e32 v3, v91
	s_mul_hi_i32 s35, s33, 0x21000
	s_mul_i32 s34, s33, 0x21000
	v_lshl_add_u64 v[2:3], s[24:25], 0, v[2:3]
	s_mov_b32 s24, 0
	s_lshl_b64 s[26:27], s[34:35], 2
	v_mov_b32_e32 v181, v91
	s_mov_b32 s25, s24
	s_add_u32 s26, s5, s26
	v_lshl_add_u64 v[2:3], v[2:3], 0, v[180:181]
	v_mov_b64_e32 v[4:5], s[24:25]
	s_addc_u32 s27, s7, s27
	s_waitcnt vmcnt(0)
	v_lshl_add_u64 v[62:63], s[34:35], 1, v[174:175]
	v_mov_b32_e32 v179, v91
	v_lshl_or_b32 v73, s36, 6, v249
	v_mov_b32_e32 v183, v91
	s_mov_b64 s[36:37], 0x2000
	s_waitcnt lgkmcnt(0)
; #define LAS __attribute__((address_space(3)))
; DI void phase_chunkB(const Args& a, LAS unsigned char* lds, int wave, int lane, int bid, int G) {
;     ...
;         asm volatile("s_waitcnt lgkmcnt(0)" ::: "memory");
; #pragma unroll
;         for (int mt = 0; mt < 4; ++mt) { *(LAS u32x2*)(Zb + r * CP + 16 * mt + 4 * q) = (u32x2){0u, 0u};
;             *(u32x2*)((bf16*)(ws + CH_ZS) + ((size_t)bh * NCK) * 4096 + (16 * iq + r) * 64 + 16 * mt + 4 * q) = (u32x2){0u, 0u}; }
;         CB_LOAD(0, 0); CB_LOAD(1, 1); CB_LOAD(2, 2);
	global_store_dwordx2 v[2:3], v[4:5], off
	v_mov_b32_e32 v164, 0
	v_mov_b32_e32 v165, 0
	v_mov_b32_e32 v166, 0
	v_mov_b32_e32 v167, 0
	global_store_dwordx2 v[2:3], v[4:5], off offset:32
	global_store_dwordx2 v[2:3], v[4:5], off offset:64
	v_mov_b32_e32 v250, 0
	v_mov_b32_e32 v251, 0
	v_mov_b32_e32 v252, 0
	v_mov_b32_e32 v253, 0
	global_store_dwordx2 v[2:3], v[4:5], off offset:96
	v_lshl_add_u64 v[18:19], v[62:63], 0, v[178:179]
	v_or_b32_e32 v104, 0x1000, v73
	v_or_b32_e32 v105, 0x1100, v73
	v_or_b32_e32 v106, 0x1200, v73
	v_or_b32_e32 v107, 0x1300, v73
	v_lshl_add_u64 v[26:27], v[62:63], 0, v[182:183]
	v_mov_b32_e32 v185, v91
	s_add_u32 s34, s26, 0x4000
	v_lshl_add_u64 v[64:65], v[62:63], 0, s[36:37]
	global_load_dwordx4 v[2:5], v[18:19], off
	global_load_dwordx4 v[6:9], v[18:19], off offset:64
	global_load_dword v10, v73, s[26:27]
	global_load_dword v11, v73, s[26:27] offset:256
	global_load_dword v12, v73, s[26:27] offset:512
	global_load_dword v13, v73, s[26:27] offset:768
	global_load_dwordx4 v[14:17], v[18:19], off offset:2048
	s_nop 0
	global_load_dwordx4 v[18:21], v[18:19], off offset:2112
	v_or_b32_e32 v132, 0x2000, v73
	global_load_dword v22, v104, s[26:27]
	global_load_dword v23, v105, s[26:27]
	global_load_dword v24, v106, s[26:27]
	global_load_dword v25, v107, s[26:27]
	global_load_dwordx4 v[38:41], v[26:27], off
	global_load_dwordx4 v[42:45], v[26:27], off offset:64
	v_or_b32_e32 v133, 0x2100, v73
	v_or_b32_e32 v134, 0x2200, v73
	v_or_b32_e32 v135, 0x2300, v73
	v_lshl_add_u64 v[26:27], v[62:63], 0, v[184:185]
	v_or_b32_e32 v144, 0x3000, v73
	v_or_b32_e32 v145, 0x3100, v73
	v_or_b32_e32 v146, 0x3200, v73
	v_or_b32_e32 v147, 0x3300, v73
	s_addc_u32 s35, s27, 0
	v_lshl_add_u64 v[50:51], v[64:65], 0, v[178:179]
	v_lshl_add_u64 v[66:67], v[64:65], 0, v[182:183]
	v_lshl_add_u64 v[64:65], v[64:65], 0, v[184:185]
	global_load_dword v54, v132, s[26:27]
	global_load_dword v55, v133, s[26:27]
	global_load_dword v56, v134, s[26:27]
	global_load_dword v57, v135, s[26:27]
	global_load_dwordx4 v[74:77], v[26:27], off
	global_load_dwordx4 v[78:81], v[26:27], off offset:64
	global_load_dword v86, v144, s[26:27]
	global_load_dword v87, v145, s[26:27]
	global_load_dword v88, v146, s[26:27]
	global_load_dword v89, v147, s[26:27]
	s_nop 0
	global_load_dwordx4 v[26:29], v[50:51], off
	global_load_dwordx4 v[30:33], v[50:51], off offset:64
	global_load_dword v34, v73, s[34:35]
	global_load_dword v35, v73, s[34:35] offset:256
	global_load_dword v36, v73, s[34:35] offset:512
	global_load_dword v37, v73, s[34:35] offset:768
	global_load_dwordx4 v[46:49], v[50:51], off offset:2048
	s_nop 0
	global_load_dwordx4 v[50:53], v[50:51], off offset:2112
	s_nop 0
	global_load_dword v58, v104, s[34:35]
	global_load_dword v59, v105, s[34:35]
	global_load_dword v60, v106, s[34:35]
	global_load_dword v61, v107, s[34:35]
	global_load_dwordx4 v[96:99], v[66:67], off
	global_load_dwordx4 v[100:103], v[66:67], off offset:64
	global_load_dword v108, v132, s[34:35]
	global_load_dword v109, v133, s[34:35]
	global_load_dword v110, v134, s[34:35]
	global_load_dword v111, v135, s[34:35]
	global_load_dwordx4 v[112:115], v[64:65], off
	global_load_dwordx4 v[116:119], v[64:65], off offset:64
	global_load_dword v120, v144, s[34:35]
	global_load_dword v121, v145, s[34:35]
	global_load_dword v122, v146, s[34:35]
	global_load_dword v123, v147, s[34:35]
	s_mov_b64 s[34:35], 0x4000
	v_lshl_add_u64 v[136:137], v[62:63], 0, s[34:35]
	s_add_u32 s26, s26, 0x8000
	v_lshl_add_u64 v[92:93], v[136:137], 0, v[178:179]
	s_addc_u32 s27, s27, 0
	global_load_dwordx4 v[62:65], v[92:93], off
	global_load_dwordx4 v[66:69], v[92:93], off offset:64
	global_load_dword v70, v73, s[26:27]
	global_load_dword v71, v73, s[26:27] offset:256
	global_load_dword v72, v73, s[26:27] offset:512
	s_nop 0
	global_load_dword v73, v73, s[26:27] offset:768
	s_nop 0
	global_load_dwordx4 v[82:85], v[92:93], off offset:2048
	s_nop 0
	global_load_dwordx4 v[92:95], v[92:93], off offset:2112
	s_nop 0
	global_load_dword v104, v104, s[26:27]
	s_nop 0
	global_load_dword v105, v105, s[26:27]
	s_nop 0
	global_load_dword v106, v106, s[26:27]
	s_nop 0
	global_load_dword v107, v107, s[26:27]
	v_lshl_add_u64 v[128:129], v[136:137], 0, v[182:183]
	v_lshl_add_u64 v[140:141], v[136:137], 0, v[184:185]
	global_load_dwordx4 v[124:127], v[128:129], off
	s_nop 0
	global_load_dwordx4 v[128:131], v[128:129], off offset:64
	s_nop 0
	global_load_dword v132, v132, s[26:27]
	s_nop 0
	global_load_dword v133, v133, s[26:27]
	s_nop 0
	global_load_dword v134, v134, s[26:27]
	s_nop 0
	global_load_dword v135, v135, s[26:27]
	s_nop 0
	global_load_dwordx4 v[136:139], v[140:141], off
	s_nop 0
	global_load_dwordx4 v[140:143], v[140:141], off offset:64
	s_nop 0
	global_load_dword v144, v144, s[26:27]
	s_nop 0
	global_load_dword v145, v145, s[26:27]
	s_nop 0
	global_load_dword v146, v146, s[26:27]
	s_nop 0
	global_load_dword v147, v147, s[26:27]
	v_mov_b32_e32 v151, v91
	v_mov_b32_e32 v153, v91
	v_mov_b32_e32 v155, v91
	v_mov_b32_e32 v157, v91
	v_mov_b32_e32 v159, v91
	v_mov_b32_e32 v161, v91
	v_mov_b32_e32 v163, v91
	v_mov_b32_e32 v149, v91
	s_mul_hi_i32 s25, s33, 0x84000
	s_mul_i32 s34, s33, 0x84000
	v_mad_i64_i32 v[190:191], s[26:27], s33, v229, v[150:151]
	v_mov_b32_e32 v151, s30
	v_or_b32_e32 v150, s31, v172
	v_mov_b32_e32 v187, s30
	v_or_b32_e32 v186, s31, v176
	v_mad_i64_i32 v[188:189], s[26:27], s33, v229, v[90:91]
	v_mad_i64_i32 v[192:193], s[26:27], s33, v229, v[152:153]
	v_mad_i64_i32 v[194:195], s[26:27], s33, v229, v[154:155]
	v_mad_i64_i32 v[196:197], s[26:27], s33, v229, v[156:157]
	v_mad_i64_i32 v[198:199], s[26:27], s33, v229, v[158:159]
	v_mad_i64_i32 v[200:201], s[26:27], s33, v229, v[160:161]
	v_mad_i64_i32 v[202:203], s[26:27], s33, v229, v[162:163]
	v_lshl_or_b32 v204, v204, 2, s34
	v_mov_b32_e32 v205, s25
	v_lshl_or_b32 v206, v206, 2, s34
	v_mov_b32_e32 v207, s25
	v_lshl_or_b32 v208, v208, 2, s34
	v_mov_b32_e32 v209, s25
	v_lshl_or_b32 v210, v210, 2, s34
	v_mov_b32_e32 v211, s25
	v_lshl_or_b32 v212, v212, 2, s34
	v_mov_b32_e32 v213, s25
	v_lshl_add_u64 v[214:215], v[150:151], 0, v[148:149]
	s_branch .LBB0_1150
.LBB0_1148:
	s_mov_b32 s25, 0x2e137000
	v_cvt_pk_bf16_f32 v160, v160, v161
	v_cvt_pk_bf16_f32 v161, v162, v163
	v_add_co_u32_e32 v162, vcc, s25, v216
	v_cvt_pk_bf16_f32 v156, v156, v157
	s_nop 0
	v_addc_co_u32_e32 v163, vcc, 0, v217, vcc
	v_cvt_pk_bf16_f32 v157, v158, v159
	v_cvt_pk_bf16_f32 v152, v152, v153
	v_cvt_pk_bf16_f32 v153, v154, v155
	v_cvt_pk_bf16_f32 v148, v148, v149
	v_cvt_pk_bf16_f32 v149, v150, v151
	global_store_dwordx2 v[162:163], v[160:161], off
	v_mov_b32_e32 v164, v160
	v_mov_b32_e32 v165, v161
	v_mov_b32_e32 v166, v156
	v_mov_b32_e32 v167, v157
	global_store_dwordx2 v[162:163], v[156:157], off offset:32
	global_store_dwordx2 v[162:163], v[152:153], off offset:64
	v_mov_b32_e32 v250, v152
	v_mov_b32_e32 v251, v153
	v_mov_b32_e32 v252, v148
	v_mov_b32_e32 v253, v149
	global_store_dwordx2 v[162:163], v[148:149], off offset:96

.LBB0_1150:
	v_add_u32_e32 v90, v233, v235
	s_cmp_gt_u32 s24, 28
	s_cselect_b64 s[26:27], -1, 0
	s_waitcnt vmcnt(26)
	v_mfma_f32_16x16x32_bf16 v[148:151], v[2:5], v[164:167], v[10:13]
	s_and_b64 vcc, exec, s[26:27]
	v_mfma_f32_16x16x32_bf16 v[160:163], v[6:9], v[250:253], v[148:151]
	s_waitcnt vmcnt(20)
	v_mfma_f32_16x16x32_bf16 v[148:151], v[14:17], v[164:167], v[22:25]
	v_mfma_f32_16x16x32_bf16 v[156:159], v[18:21], v[250:253], v[148:151]
	s_waitcnt vmcnt(14)
	v_mfma_f32_16x16x32_bf16 v[148:151], v[38:41], v[164:167], v[54:57]
	s_waitcnt vmcnt(8)
	v_mfma_f32_16x16x32_bf16 v[152:155], v[74:77], v[164:167], v[86:89]
	v_mfma_f32_16x16x32_bf16 v[148:151], v[42:45], v[250:253], v[148:151]
	v_mfma_f32_16x16x32_bf16 v[152:155], v[78:81], v[250:253], v[152:155]
	s_cbranch_vccnz .LBB0_1152
	v_lshl_add_u64 v[38:39], s[8:9], 0, v[186:187]
	v_add_co_u32_e32 v18, vcc, 0x27e37000, v38
	v_lshl_add_u64 v[10:11], s[8:9], 0, v[212:213]
	s_nop 0
	v_addc_co_u32_e32 v19, vcc, 0, v39, vcc
	v_add_co_u32_e32 v14, vcc, 0x28ebd000, v10
	v_lshl_add_u64 v[22:23], s[8:9], 0, v[210:211]
	s_nop 0
	v_addc_co_u32_e32 v15, vcc, 0, v11, vcc
	v_add_co_u32_e32 v22, vcc, 0x28ebd000, v22
	v_lshl_add_u64 v[24:25], s[8:9], 0, v[208:209]
	s_nop 0
	v_addc_co_u32_e32 v23, vcc, 0, v23, vcc
	v_add_co_u32_e32 v24, vcc, 0x28ebd000, v24
	global_load_dwordx4 v[2:5], v[18:19], off
	global_load_dwordx4 v[6:9], v[18:19], off offset:64
	v_addc_co_u32_e32 v25, vcc, 0, v25, vcc
	global_load_dword v10, v[14:15], off
	global_load_dword v11, v[14:15], off offset:256
	global_load_dword v12, v[14:15], off offset:512
	global_load_dword v13, v[14:15], off offset:768
	s_nop 0
	global_load_dwordx4 v[14:17], v[18:19], off offset:2048
	s_nop 0
	global_load_dwordx4 v[18:21], v[18:19], off offset:2112
	v_lshl_add_u64 v[40:41], s[8:9], 0, v[204:205]
	global_load_dword v22, v[22:23], off
	v_lshl_add_u64 v[54:55], s[8:9], 0, v[202:203]
	global_load_dword v23, v[24:25], off
	v_lshl_add_u64 v[24:25], s[8:9], 0, v[206:207]
	v_add_co_u32_e32 v24, vcc, 0x28ebd000, v24
	v_lshl_add_u64 v[56:57], s[8:9], 0, v[200:201]
	s_nop 0
	v_addc_co_u32_e32 v25, vcc, 0, v25, vcc
	v_add_co_u32_e32 v40, vcc, 0x28ebd000, v40
	global_load_dword v24, v[24:25], off
	s_nop 0
	v_addc_co_u32_e32 v41, vcc, 0, v41, vcc
	v_add_co_u32_e32 v78, vcc, 0x27e38000, v38
	global_load_dword v25, v[40:41], off
	s_nop 0
	v_addc_co_u32_e32 v79, vcc, 0, v39, vcc
	v_add_co_u32_e32 v54, vcc, 0x28ebd000, v54
	global_load_dwordx4 v[38:41], v[78:79], off
	global_load_dwordx4 v[42:45], v[78:79], off offset:64
	v_addc_co_u32_e32 v55, vcc, 0, v55, vcc
	v_add_co_u32_e32 v56, vcc, 0x28ebd000, v56
	global_load_dword v54, v[54:55], off
	s_nop 0
	v_addc_co_u32_e32 v57, vcc, 0, v57, vcc
	global_load_dword v55, v[56:57], off
	v_lshl_add_u64 v[56:57], s[8:9], 0, v[198:199]
	v_add_co_u32_e32 v56, vcc, 0x28ebd000, v56
	v_lshl_add_u64 v[74:75], s[8:9], 0, v[196:197]
	s_nop 0
	v_addc_co_u32_e32 v57, vcc, 0, v57, vcc
	v_add_co_u32_e32 v74, vcc, 0x28ebd000, v74
	v_lshl_add_u64 v[86:87], s[8:9], 0, v[194:195]
	s_nop 0
	v_addc_co_u32_e32 v75, vcc, 0, v75, vcc
	v_add_co_u32_e32 v86, vcc, 0x28ebd000, v86
	v_lshl_add_u64 v[88:89], s[8:9], 0, v[192:193]
	s_nop 0
	v_addc_co_u32_e32 v87, vcc, 0, v87, vcc
	v_add_co_u32_e32 v88, vcc, 0x28ebd000, v88
	global_load_dword v56, v[56:57], off
	s_nop 0
	v_addc_co_u32_e32 v89, vcc, 0, v89, vcc
	global_load_dword v57, v[74:75], off
	s_nop 0
	global_load_dwordx4 v[74:77], v[78:79], off offset:2048
	s_nop 0
	global_load_dwordx4 v[78:81], v[78:79], off offset:2112
	v_lshl_add_u64 v[164:165], s[8:9], 0, v[188:189]
	global_load_dword v86, v[86:87], off
	s_nop 0
	global_load_dword v87, v[88:89], off
	v_lshl_add_u64 v[88:89], s[8:9], 0, v[190:191]
	v_add_co_u32_e32 v88, vcc, 0x28ebd000, v88
	s_nop 1
	v_addc_co_u32_e32 v89, vcc, 0, v89, vcc
	v_add_co_u32_e32 v164, vcc, 0x28ebd000, v164
	global_load_dword v88, v[88:89], off
	s_nop 0
	v_addc_co_u32_e32 v165, vcc, 0, v165, vcc
	global_load_dword v89, v[164:165], off
.LBB0_1152:
	v_lshl_add_u64 v[216:217], s[8:9], 0, v[214:215]
	s_mov_b32 s25, 0x2e133000
	v_cvt_pk_bf16_f32 v160, v160, v161
	v_cvt_pk_bf16_f32 v161, v162, v163
	v_add_co_u32_e32 v162, vcc, s25, v216
	v_cvt_pk_bf16_f32 v156, v156, v157
	s_nop 0
	v_addc_co_u32_e32 v163, vcc, 0, v217, vcc
	v_cvt_pk_bf16_f32 v157, v158, v159
	v_cvt_pk_bf16_f32 v148, v148, v149
	v_cvt_pk_bf16_f32 v149, v150, v151
	v_cvt_pk_bf16_f32 v150, v152, v153
	v_cvt_pk_bf16_f32 v151, v154, v155
	global_store_dwordx2 v[162:163], v[160:161], off
	v_mov_b32_e32 v164, v160
	v_mov_b32_e32 v165, v161
	v_mov_b32_e32 v166, v156
	v_mov_b32_e32 v167, v157
	global_store_dwordx2 v[162:163], v[156:157], off offset:32
	global_store_dwordx2 v[162:163], v[148:149], off offset:64
	v_mov_b32_e32 v250, v148
	v_mov_b32_e32 v251, v149
	v_mov_b32_e32 v252, v150
	v_mov_b32_e32 v253, v151
	global_store_dwordx2 v[162:163], v[150:151], off offset:96
	s_waitcnt vmcnt(46)
	v_mfma_f32_16x16x32_bf16 v[152:155], v[26:29], v[164:167], v[34:37]
	s_cmp_gt_u32 s24, 27
	s_waitcnt lgkmcnt(0)
	v_mfma_f32_16x16x32_bf16 v[160:163], v[30:33], v[250:253], v[152:155]
	s_waitcnt vmcnt(40)
	v_mfma_f32_16x16x32_bf16 v[152:155], v[46:49], v[164:167], v[58:61]
	v_mfma_f32_16x16x32_bf16 v[156:159], v[50:53], v[250:253], v[152:155]
	s_waitcnt vmcnt(34)
	v_mfma_f32_16x16x32_bf16 v[152:155], v[96:99], v[164:167], v[108:111]
	s_waitcnt vmcnt(8)
	v_mfma_f32_16x16x32_bf16 v[148:151], v[112:115], v[164:167], v[120:123]
	v_mfma_f32_16x16x32_bf16 v[152:155], v[100:103], v[250:253], v[152:155]
	v_mfma_f32_16x16x32_bf16 v[148:151], v[116:119], v[250:253], v[148:151]
	s_cbranch_scc1 .LBB0_1154
	v_lshl_add_u64 v[96:97], s[8:9], 0, v[186:187]
	v_add_co_u32_e32 v50, vcc, 0x27e39000, v96
	v_lshl_add_u64 v[34:35], s[8:9], 0, v[212:213]
	s_nop 0
	v_addc_co_u32_e32 v51, vcc, 0, v97, vcc
	v_add_co_u32_e32 v46, vcc, 0x28ec1000, v34
	v_lshl_add_u64 v[58:59], s[8:9], 0, v[210:211]
	s_nop 0
	v_addc_co_u32_e32 v47, vcc, 0, v35, vcc
	v_add_co_u32_e32 v58, vcc, 0x28ec1000, v58
	v_lshl_add_u64 v[60:61], s[8:9], 0, v[208:209]
	s_nop 0
	v_addc_co_u32_e32 v59, vcc, 0, v59, vcc
	v_add_co_u32_e32 v60, vcc, 0x28ec1000, v60
	global_load_dwordx4 v[26:29], v[50:51], off
	global_load_dwordx4 v[30:33], v[50:51], off offset:64
	v_addc_co_u32_e32 v61, vcc, 0, v61, vcc
	global_load_dword v34, v[46:47], off
	global_load_dword v35, v[46:47], off offset:256
	global_load_dword v36, v[46:47], off offset:512
	global_load_dword v37, v[46:47], off offset:768
	s_nop 0
	global_load_dwordx4 v[46:49], v[50:51], off offset:2048
	s_nop 0
	global_load_dwordx4 v[50:53], v[50:51], off offset:2112
	v_lshl_add_u64 v[98:99], s[8:9], 0, v[204:205]
	global_load_dword v58, v[58:59], off
	v_lshl_add_u64 v[108:109], s[8:9], 0, v[202:203]
	global_load_dword v59, v[60:61], off
	v_lshl_add_u64 v[60:61], s[8:9], 0, v[206:207]
	v_add_co_u32_e32 v60, vcc, 0x28ec1000, v60
	v_lshl_add_u64 v[110:111], s[8:9], 0, v[200:201]
	s_nop 0
	v_addc_co_u32_e32 v61, vcc, 0, v61, vcc
	v_add_co_u32_e32 v98, vcc, 0x28ec1000, v98
	global_load_dword v60, v[60:61], off
	s_nop 0
	v_addc_co_u32_e32 v99, vcc, 0, v99, vcc
	v_add_co_u32_e32 v116, vcc, 0x27e3a000, v96
	global_load_dword v61, v[98:99], off
	s_nop 0
	v_addc_co_u32_e32 v117, vcc, 0, v97, vcc
	v_add_co_u32_e32 v108, vcc, 0x28ec1000, v108
	global_load_dwordx4 v[96:99], v[116:117], off
	global_load_dwordx4 v[100:103], v[116:117], off offset:64
	v_addc_co_u32_e32 v109, vcc, 0, v109, vcc
	v_add_co_u32_e32 v110, vcc, 0x28ec1000, v110
	global_load_dword v108, v[108:109], off
	s_nop 0
	v_addc_co_u32_e32 v111, vcc, 0, v111, vcc
	global_load_dword v109, v[110:111], off
	v_lshl_add_u64 v[110:111], s[8:9], 0, v[198:199]
	v_add_co_u32_e32 v110, vcc, 0x28ec1000, v110
	v_lshl_add_u64 v[112:113], s[8:9], 0, v[196:197]
	s_nop 0
	v_addc_co_u32_e32 v111, vcc, 0, v111, vcc
	v_add_co_u32_e32 v112, vcc, 0x28ec1000, v112
	v_lshl_add_u64 v[120:121], s[8:9], 0, v[194:195]
	s_nop 0
	v_addc_co_u32_e32 v113, vcc, 0, v113, vcc
	v_add_co_u32_e32 v120, vcc, 0x28ec1000, v120
	v_lshl_add_u64 v[122:123], s[8:9], 0, v[192:193]
	s_nop 0
	v_addc_co_u32_e32 v121, vcc, 0, v121, vcc
	v_add_co_u32_e32 v122, vcc, 0x28ec1000, v122
	global_load_dword v110, v[110:111], off
	s_nop 0
	v_addc_co_u32_e32 v123, vcc, 0, v123, vcc
	global_load_dword v111, v[112:113], off
	s_nop 0
	global_load_dwordx4 v[112:115], v[116:117], off offset:2048
	s_nop 0
	global_load_dwordx4 v[116:119], v[116:117], off offset:2112
	v_lshl_add_u64 v[164:165], s[8:9], 0, v[188:189]
	global_load_dword v120, v[120:121], off
	s_nop 0
	global_load_dword v121, v[122:123], off
	v_lshl_add_u64 v[122:123], s[8:9], 0, v[190:191]
	v_add_co_u32_e32 v122, vcc, 0x28ec1000, v122
	s_nop 1
	v_addc_co_u32_e32 v123, vcc, 0, v123, vcc
	v_add_co_u32_e32 v164, vcc, 0x28ec1000, v164
	global_load_dword v122, v[122:123], off
	s_nop 0
	v_addc_co_u32_e32 v165, vcc, 0, v165, vcc
	global_load_dword v123, v[164:165], off
; #define LAS __attribute__((address_space(3)))
; DI void phase_chunkB(const Args& a, LAS unsigned char* lds, int wave, int lane, int bid, int G) {
;     ...
;         asm volatile("s_waitcnt lgkmcnt(0)" ::: "memory");
; #pragma unroll
;         for (int mt = 0; mt < 4; ++mt) { *(LAS u32x2*)(Zb + r * CP + 16 * mt + 4 * q) = (u32x2){0u, 0u};
;             *(u32x2*)((bf16*)(ws + CH_ZS) + ((size_t)bh * NCK) * 4096 + (16 * iq + r) * 64 + 16 * mt + 4 * q) = (u32x2){0u, 0u}; }
;         CB_LOAD(0, 0); CB_LOAD(1, 1); CB_LOAD(2, 2);
;         static_assert(NCK - 1 >= 3, "three steps are requested before the loop");
; #pragma unroll 1
;         for (int c = 0; c < NCK - 1; c += 3) { CB_STEP(0, c); CB_STEP(1, c + 1); CB_STEP(2, c + 2); }
.LBB0_1154:
	s_mov_b32 s25, 0x2e135000
	v_cvt_pk_bf16_f32 v160, v160, v161
	v_cvt_pk_bf16_f32 v161, v162, v163
	v_add_co_u32_e32 v162, vcc, s25, v216
	v_cvt_pk_bf16_f32 v156, v156, v157
	s_nop 0
	v_addc_co_u32_e32 v163, vcc, 0, v217, vcc
	v_cvt_pk_bf16_f32 v157, v158, v159
	v_cvt_pk_bf16_f32 v152, v152, v153
	v_cvt_pk_bf16_f32 v153, v154, v155
	v_cvt_pk_bf16_f32 v148, v148, v149
	v_cvt_pk_bf16_f32 v149, v150, v151
	s_cmp_gt_u32 s24, 29
	global_store_dwordx2 v[162:163], v[160:161], off
	v_mov_b32_e32 v164, v160
	v_mov_b32_e32 v165, v161
	v_mov_b32_e32 v166, v156
	v_mov_b32_e32 v167, v157
	global_store_dwordx2 v[162:163], v[156:157], off offset:32
	global_store_dwordx2 v[162:163], v[152:153], off offset:64
	v_mov_b32_e32 v250, v152
	v_mov_b32_e32 v251, v153
	v_mov_b32_e32 v252, v148
	v_mov_b32_e32 v253, v149
	global_store_dwordx2 v[162:163], v[148:149], off offset:96
	s_cbranch_scc1 .LBB0_1149
	s_cmp_gt_u32 s24, 26
	s_waitcnt vmcnt(26)
	v_mfma_f32_16x16x32_bf16 v[152:155], v[62:65], v[164:167], v[70:73]
	v_mfma_f32_16x16x32_bf16 v[160:163], v[66:69], v[250:253], v[152:155]
	s_waitcnt vmcnt(20)
	v_mfma_f32_16x16x32_bf16 v[152:155], v[82:85], v[164:167], v[104:107]
	v_mfma_f32_16x16x32_bf16 v[156:159], v[92:95], v[250:253], v[152:155]
	s_waitcnt vmcnt(14)
	v_mfma_f32_16x16x32_bf16 v[152:155], v[124:127], v[164:167], v[132:135]
	s_waitcnt vmcnt(8)
	v_mfma_f32_16x16x32_bf16 v[148:151], v[136:139], v[164:167], v[144:147]
	v_mfma_f32_16x16x32_bf16 v[152:155], v[128:131], v[250:253], v[152:155]
	v_mfma_f32_16x16x32_bf16 v[148:151], v[140:143], v[250:253], v[148:151]
	s_cbranch_scc1 .LBB0_1148
	v_lshl_add_u64 v[124:125], s[8:9], 0, v[186:187]
	v_add_co_u32_e32 v92, vcc, 0x27e3b000, v124
	v_lshl_add_u64 v[70:71], s[8:9], 0, v[212:213]
	s_nop 0
	v_addc_co_u32_e32 v93, vcc, 0, v125, vcc
	v_add_co_u32_e32 v82, vcc, 0x28ec5000, v70
	v_lshl_add_u64 v[104:105], s[8:9], 0, v[210:211]
	s_nop 0
	v_addc_co_u32_e32 v83, vcc, 0, v71, vcc
	v_add_co_u32_e32 v104, vcc, 0x28ec5000, v104
	v_lshl_add_u64 v[106:107], s[8:9], 0, v[208:209]
	s_nop 0
	v_addc_co_u32_e32 v105, vcc, 0, v105, vcc
	v_add_co_u32_e32 v106, vcc, 0x28ec5000, v106
	global_load_dwordx4 v[62:65], v[92:93], off
	global_load_dwordx4 v[66:69], v[92:93], off offset:64
	v_addc_co_u32_e32 v107, vcc, 0, v107, vcc
	global_load_dword v70, v[82:83], off
	global_load_dword v71, v[82:83], off offset:256
	global_load_dword v72, v[82:83], off offset:512
	global_load_dword v73, v[82:83], off offset:768
	s_nop 0
	global_load_dwordx4 v[82:85], v[92:93], off offset:2048
	s_nop 0
	global_load_dwordx4 v[92:95], v[92:93], off offset:2112
	v_lshl_add_u64 v[126:127], s[8:9], 0, v[204:205]
	global_load_dword v104, v[104:105], off
	v_lshl_add_u64 v[132:133], s[8:9], 0, v[202:203]
	global_load_dword v105, v[106:107], off
	v_lshl_add_u64 v[106:107], s[8:9], 0, v[206:207]
	v_add_co_u32_e32 v106, vcc, 0x28ec5000, v106
	v_lshl_add_u64 v[134:135], s[8:9], 0, v[200:201]
	s_nop 0
	v_addc_co_u32_e32 v107, vcc, 0, v107, vcc
	v_add_co_u32_e32 v126, vcc, 0x28ec5000, v126
	global_load_dword v106, v[106:107], off
	s_nop 0
	v_addc_co_u32_e32 v127, vcc, 0, v127, vcc
	v_add_co_u32_e32 v140, vcc, 0x27e3c000, v124
	global_load_dword v107, v[126:127], off
	s_nop 0
	v_addc_co_u32_e32 v141, vcc, 0, v125, vcc
	v_add_co_u32_e32 v132, vcc, 0x28ec5000, v132
	global_load_dwordx4 v[124:127], v[140:141], off
	global_load_dwordx4 v[128:131], v[140:141], off offset:64
	v_addc_co_u32_e32 v133, vcc, 0, v133, vcc
	v_add_co_u32_e32 v134, vcc, 0x28ec5000, v134
	global_load_dword v132, v[132:133], off
	s_nop 0
	v_addc_co_u32_e32 v135, vcc, 0, v135, vcc
	global_load_dword v133, v[134:135], off
	v_lshl_add_u64 v[134:135], s[8:9], 0, v[198:199]
	v_add_co_u32_e32 v134, vcc, 0x28ec5000, v134
	v_lshl_add_u64 v[136:137], s[8:9], 0, v[196:197]
	s_nop 0
	v_addc_co_u32_e32 v135, vcc, 0, v135, vcc
	v_add_co_u32_e32 v136, vcc, 0x28ec5000, v136
	v_lshl_add_u64 v[144:145], s[8:9], 0, v[194:195]
	s_nop 0
	v_addc_co_u32_e32 v137, vcc, 0, v137, vcc
	v_add_co_u32_e32 v144, vcc, 0x28ec5000, v144
	v_lshl_add_u64 v[146:147], s[8:9], 0, v[192:193]
	s_nop 0
	v_addc_co_u32_e32 v145, vcc, 0, v145, vcc
	v_add_co_u32_e32 v146, vcc, 0x28ec5000, v146
	global_load_dword v134, v[134:135], off
	s_nop 0
	v_addc_co_u32_e32 v147, vcc, 0, v147, vcc
	global_load_dword v135, v[136:137], off
	s_nop 0
	global_load_dwordx4 v[136:139], v[140:141], off offset:2048
	s_nop 0
	global_load_dwordx4 v[140:143], v[140:141], off offset:2112
	v_lshl_add_u64 v[164:165], s[8:9], 0, v[188:189]
	global_load_dword v144, v[144:145], off
	s_nop 0
	global_load_dword v145, v[146:147], off
	v_lshl_add_u64 v[146:147], s[8:9], 0, v[190:191]
	v_add_co_u32_e32 v146, vcc, 0x28ec5000, v146
	s_nop 1
	v_addc_co_u32_e32 v147, vcc, 0, v147, vcc
	v_add_co_u32_e32 v164, vcc, 0x28ec5000, v164
	global_load_dword v146, v[146:147], off
	s_nop 0
	v_addc_co_u32_e32 v165, vcc, 0, v165, vcc
	global_load_dword v147, v[164:165], off
	s_branch .LBB0_1148
